# v040 + 8 now-dead compare instructions of hipcc's old bitonic layer removed from the topk unit
# speedup vs baseline: 1.0091x; 1.0003x over previous
; #define LAS __attribute__((address_space(3)))
; __device__ __forceinline__ f32x4 mfma16(bf16x8 a, bf16x8 b, f32x4 c) { return __builtin_amdgcn_mfma_f32_16x16x32_bf16(a, b, c, 0, 0, 0); }
; __device__ __forceinline__ void topk_phase(LAS unsigned char* lds, const bf16_t* qp, const bf16_t* keys, const float* SU, const float* SV, int* sel_e, float* sel_g, float* sel_su, int G, int b) {
;     ...
;         const int tt = gu.pm * 2 + (ui & 1), h = gu.pn;
;         const int tok = tt * 128 + wid * 16 + fr;
;         if ((ui & 1) == 0) {
;             if (ui == 0) {
;                 const bf16_t* src = keys + (size_t)h * 2 * 16384 + (size_t)krow * 128 + khf * 64;
; #pragma unroll
;                 for (int q8 = 0; q8 < 8; ++q8) kpre[q8] = *(const u32x4*)(src + q8 * 8);
;             } else __syncthreads();
;             LAS bf16_t* dst = KL + krow * 136 + khf * 64;
; #pragma unroll
;             for (int q8 = 0; q8 < 8; ++q8) *(LAS u32x4*)(dst + q8 * 8) = kpre[q8];
;             __syncthreads();
;         } else {
;             pg8::Unit gn;
;             if (SO.next((ui + 1) >> 1, gn)) { const bf16_t* src = keys + (size_t)gn.pn * 2 * 16384 + (size_t)krow * 128 + khf * 64;
; #pragma unroll
;                 for (int q8 = 0; q8 < 8; ++q8) kpre[q8] = *(const u32x4*)(src + q8 * 8); }
;         }
;         unsigned T[2][16];
; #pragma unroll
;         for (int p = 0; p < 2; ++p) {
;             f32x4 acc[8];
; #pragma unroll
;             for (int mt = 0; mt < 8; ++mt) acc[mt] = (f32x4){0.f, 0.f, 0.f, 0.f};
;             bf16x8 bq[4];
; #pragma unroll
;             for (int ks = 0; ks < 4; ++ks) bq[ks] = *(const bf16x8*)(qp + (size_t)tok * D_ + h * 256 + p * 128 + ks * 32 + fq * 8);
;             const LAS bf16_t* kb = KL + p * 128 * 136;
; #pragma unroll
;             for (int mt = 0; mt < 8; ++mt)
; #pragma unroll
;                 for (int ks = 0; ks < 4; ++ks) { const bf16x8 a = *(const LAS bf16x8*)(kb + (mt * 16 + fr) * 136 + ks * 32 + fq * 8); acc[mt] = mfma16(a, bq[ks], acc[mt]); }
.LBB0_659:
	s_and_b32 s0, s52, 1
	s_lshl_b32 s1, s64, 8
	s_lshl_b32 s0, s0, 7
	s_or_b32 s0, s1, s0
	v_add_u32_e32 v94, s0, v85
	v_ashrrev_i32_e32 v95, 31, v94
	v_lshlrev_b64 v[34:35], 12, v[94:95]
	s_lshl_b32 s0, s56, 8
	v_lshl_add_u64 v[34:35], s[74:75], 0, v[34:35]
	s_ashr_i32 s1, s0, 31
	v_lshl_add_u64 v[34:35], s[0:1], 1, v[34:35]
	v_lshl_add_u64 v[96:97], v[34:35], 0, v[78:79]
	global_load_dwordx4 v[66:69], v[96:97], off
	global_load_dwordx4 v[62:65], v[96:97], off offset:64
	global_load_dwordx4 v[58:61], v[96:97], off offset:128
	global_load_dwordx4 v[54:57], v[96:97], off offset:192
	v_add_u32_e32 v138, v87, v89
	s_movk_i32 s0, 0xff
	ds_read_b128 v[174:177], v138 offset:32768
	ds_read_b128 v[178:181], v138 offset:37120
	ds_read_b128 v[182:185], v138 offset:41472
	ds_read_b128 v[186:189], v138 offset:45824
	ds_read_b128 v[190:193], v138 offset:50176
	ds_read_b128 v[194:197], v138 offset:54528
	ds_read_b128 v[198:201], v138 offset:58880
	ds_read_b128 v[216:219], v138 offset:32832
	ds_read_b128 v[220:223], v138 offset:37184
	ds_read_b128 v[224:227], v138 offset:41536
	ds_read_b128 v[228:231], v138 offset:45888
	ds_read_b128 v[232:235], v138 offset:50240
	ds_read_b128 v[236:239], v138 offset:54592
	ds_read_b128 v[244:247], v138 offset:58944
	ds_read_b128 v[248:251], v138 offset:32896
	ds_read_b128 v[252:255], v138 offset:37248
	s_waitcnt vmcnt(3) lgkmcnt(15)
	v_mfma_f32_16x16x32_bf16 v[46:49], v[174:177], v[66:69], 0
	ds_read_b128 v[174:177], v138 offset:41600
	s_waitcnt lgkmcnt(15)
	v_mfma_f32_16x16x32_bf16 v[34:37], v[178:181], v[66:69], 0
	ds_read_b128 v[178:181], v138 offset:45952
	s_waitcnt lgkmcnt(15)
	v_mfma_f32_16x16x32_bf16 v[38:41], v[182:185], v[66:69], 0
	ds_read_b128 v[182:185], v138 offset:50304
	s_waitcnt lgkmcnt(15)
	v_mfma_f32_16x16x32_bf16 v[42:45], v[186:189], v[66:69], 0
	ds_read_b128 v[186:189], v138 offset:54656
	s_waitcnt lgkmcnt(15)
	v_mfma_f32_16x16x32_bf16 v[70:73], v[190:193], v[66:69], 0
	ds_read_b128 v[190:193], v138 offset:59008
	s_waitcnt lgkmcnt(15)
	v_mfma_f32_16x16x32_bf16 v[50:53], v[194:197], v[66:69], 0
	ds_read_b128 v[194:197], v138 offset:32960
	s_waitcnt lgkmcnt(15)
	v_mfma_f32_16x16x32_bf16 v[74:77], v[198:201], v[66:69], 0
	ds_read_b128 v[198:201], v138 offset:37312
	s_waitcnt vmcnt(2) lgkmcnt(15)
	v_mfma_f32_16x16x32_bf16 v[46:49], v[216:219], v[62:65], v[46:49]
	ds_read_b128 v[216:219], v138 offset:41664
	s_waitcnt lgkmcnt(15)
	v_mfma_f32_16x16x32_bf16 v[34:37], v[220:223], v[62:65], v[34:37]
	ds_read_b128 v[220:223], v138 offset:46016
	s_waitcnt lgkmcnt(15)
	v_mfma_f32_16x16x32_bf16 v[38:41], v[224:227], v[62:65], v[38:41]
	ds_read_b128 v[224:227], v138 offset:50368
	s_waitcnt lgkmcnt(15)
	v_mfma_f32_16x16x32_bf16 v[42:45], v[228:231], v[62:65], v[42:45]
	ds_read_b128 v[228:231], v138 offset:54720
	s_waitcnt lgkmcnt(15)
	v_mfma_f32_16x16x32_bf16 v[70:73], v[232:235], v[62:65], v[70:73]
	ds_read_b128 v[232:235], v138 offset:59072
	s_waitcnt lgkmcnt(15)
	v_mfma_f32_16x16x32_bf16 v[50:53], v[236:239], v[62:65], v[50:53]
	ds_read_b128 v[236:239], v138 offset:63232
	s_waitcnt lgkmcnt(15)
	v_mfma_f32_16x16x32_bf16 v[74:77], v[244:247], v[62:65], v[74:77]
	ds_read_b128 v[244:247], v138 offset:63296
	s_waitcnt vmcnt(1) lgkmcnt(15)
	v_mfma_f32_16x16x32_bf16 v[46:49], v[248:251], v[58:61], v[46:49]
	ds_read_b128 v[248:251], v138 offset:63360
	s_waitcnt lgkmcnt(15)
	v_mfma_f32_16x16x32_bf16 v[34:37], v[252:255], v[58:61], v[34:37]
	ds_read_b128 v[252:255], v138 offset:63424
	s_waitcnt lgkmcnt(15)
	v_mfma_f32_16x16x32_bf16 v[38:41], v[174:177], v[58:61], v[38:41]
	s_waitcnt lgkmcnt(14)
	v_mfma_f32_16x16x32_bf16 v[42:45], v[178:181], v[58:61], v[42:45]
	s_waitcnt lgkmcnt(13)
	v_mfma_f32_16x16x32_bf16 v[70:73], v[182:185], v[58:61], v[70:73]
	s_waitcnt lgkmcnt(12)
	v_mfma_f32_16x16x32_bf16 v[50:53], v[186:189], v[58:61], v[50:53]
	s_waitcnt lgkmcnt(11)
	v_mfma_f32_16x16x32_bf16 v[74:77], v[190:193], v[58:61], v[74:77]
	s_waitcnt vmcnt(0) lgkmcnt(10)
	v_mfma_f32_16x16x32_bf16 v[46:49], v[194:197], v[54:57], v[46:49]
	s_waitcnt lgkmcnt(9)
	v_mfma_f32_16x16x32_bf16 v[34:37], v[198:201], v[54:57], v[34:37]
	s_waitcnt lgkmcnt(8)
	v_mfma_f32_16x16x32_bf16 v[38:41], v[216:219], v[54:57], v[38:41]
	s_waitcnt lgkmcnt(7)
	v_mfma_f32_16x16x32_bf16 v[42:45], v[220:223], v[54:57], v[42:45]
	s_waitcnt lgkmcnt(6)
	v_mfma_f32_16x16x32_bf16 v[70:73], v[224:227], v[54:57], v[70:73]
	s_waitcnt lgkmcnt(5)
	v_mfma_f32_16x16x32_bf16 v[50:53], v[228:231], v[54:57], v[50:53]
	s_waitcnt lgkmcnt(4)
	v_mfma_f32_16x16x32_bf16 v[74:77], v[232:235], v[54:57], v[74:77]
	s_waitcnt lgkmcnt(3)
	v_mfma_f32_16x16x32_bf16 v[66:69], v[236:239], v[66:69], 0
	s_waitcnt lgkmcnt(2)
	v_mfma_f32_16x16x32_bf16 v[62:65], v[244:247], v[62:65], v[66:69]
	s_waitcnt lgkmcnt(1)
	v_mfma_f32_16x16x32_bf16 v[58:61], v[248:251], v[58:61], v[62:65]
	s_waitcnt lgkmcnt(0)
; __device__ __forceinline__ unsigned mono(float f) { const unsigned u = __float_as_uint(f); return (u & 0x80000000u) ? ~u : (u ^ 0x80000000u); }
; __device__ __forceinline__ void topk_phase(LAS unsigned char* lds, const bf16_t* qp, const bf16_t* keys, const float* SU, const float* SV, int* sel_e, float* sel_g, float* sel_su, int G, int b) {
;     ...
;             unsigned lo16[16];
; #pragma unroll
;             for (int mt = 0; mt < 4; ++mt)
; #pragma unroll
;                 for (int r = 0; r < 4; ++r) {
;                     T[p][mt * 4 + r] = (mono(acc[mt][r]) & ~127u) | (unsigned)(127 - (mt * 16 + fq * 4 + r));
;                     lo16[mt * 4 + r] = (mono(acc[mt + 4][r]) & ~127u) | (unsigned)(127 - ((mt + 4) * 16 + fq * 4 + r));
;                 }
;             SN_SORT16(T[p]); SN_SORT16(lo16);
	v_mfma_f32_16x16x32_bf16 v[54:57], v[252:255], v[54:57], v[58:61]
	s_nop 2
	v_ashrrev_i32_e32 v58, 31, v46
	v_bitop3_b32 v46, v46, v58, v132 bitop3:0x1e
	v_and_or_b32 v46, v46, s53, v98
	v_ashrrev_i32_e32 v58, 31, v70
	v_bitop3_b32 v58, v70, v58, v132 bitop3:0x1e
	v_and_or_b32 v58, v58, s53, v99
	v_ashrrev_i32_e32 v59, 31, v47
	v_bitop3_b32 v47, v47, v59, v132 bitop3:0x1e
	v_and_or_b32 v47, v47, s53, v100
	v_ashrrev_i32_e32 v59, 31, v71
	v_bitop3_b32 v59, v71, v59, v132 bitop3:0x1e
	v_and_or_b32 v59, v59, s53, v101
	v_ashrrev_i32_e32 v60, 31, v48
	v_bitop3_b32 v48, v48, v60, v132 bitop3:0x1e
	v_and_or_b32 v48, v48, s53, v102
	v_ashrrev_i32_e32 v60, 31, v72
	v_bitop3_b32 v60, v72, v60, v132 bitop3:0x1e
	v_and_or_b32 v60, v60, s53, v103
	v_ashrrev_i32_e32 v61, 31, v49
	v_bitop3_b32 v49, v49, v61, v132 bitop3:0x1e
	v_and_or_b32 v49, v49, s53, v104
	v_ashrrev_i32_e32 v61, 31, v73
	v_bitop3_b32 v61, v73, v61, v132 bitop3:0x1e
	v_and_or_b32 v61, v61, s53, v105
	v_ashrrev_i32_e32 v62, 31, v34
	v_bitop3_b32 v34, v34, v62, v132 bitop3:0x1e
	v_and_or_b32 v34, v34, s53, v106
	v_ashrrev_i32_e32 v62, 31, v50
	v_bitop3_b32 v50, v50, v62, v132 bitop3:0x1e
	v_and_or_b32 v50, v50, s53, v107
	v_ashrrev_i32_e32 v62, 31, v35
	v_bitop3_b32 v35, v35, v62, v132 bitop3:0x1e
	v_and_or_b32 v35, v35, s53, v108
	v_ashrrev_i32_e32 v62, 31, v51
	v_bitop3_b32 v51, v51, v62, v132 bitop3:0x1e
	v_and_or_b32 v51, v51, s53, v109
	v_ashrrev_i32_e32 v62, 31, v36
	v_bitop3_b32 v36, v36, v62, v132 bitop3:0x1e
	v_and_or_b32 v36, v36, s53, v110
	v_ashrrev_i32_e32 v62, 31, v52
	v_bitop3_b32 v52, v52, v62, v132 bitop3:0x1e
	v_and_or_b32 v52, v52, s53, v111
	v_ashrrev_i32_e32 v62, 31, v37
	v_bitop3_b32 v37, v37, v62, v132 bitop3:0x1e
	v_and_or_b32 v37, v37, s53, v112
	v_ashrrev_i32_e32 v62, 31, v53
	v_bitop3_b32 v53, v53, v62, v132 bitop3:0x1e
	v_and_or_b32 v53, v53, s53, v113
	v_ashrrev_i32_e32 v62, 31, v38
	v_bitop3_b32 v38, v38, v62, v132 bitop3:0x1e
	v_and_or_b32 v38, v38, s53, v114
	v_ashrrev_i32_e32 v62, 31, v74
	v_bitop3_b32 v62, v74, v62, v132 bitop3:0x1e
	v_max_u32_e32 v74, v58, v59
	v_ashrrev_i32_e32 v63, 31, v39
	v_cmp_lt_i32_e32 vcc, -1, v75
	v_bitop3_b32 v39, v39, v63, v132 bitop3:0x1e
	v_min_u32_e32 v58, v58, v59
	v_cndmask_b32_e32 v63, -1, v132, vcc
	v_max_u32_e32 v59, v60, v61
	v_min_u32_e32 v60, v60, v61
	v_ashrrev_i32_e32 v64, 31, v40
	v_cmp_lt_i32_e32 vcc, -1, v76
	v_bitop3_b32 v40, v40, v64, v132 bitop3:0x1e
	v_max_u32_e32 v61, v74, v59
	v_cndmask_b32_e32 v64, -1, v132, vcc
	v_min_u32_e32 v59, v74, v59
	v_max_u32_e32 v74, v58, v60
	v_ashrrev_i32_e32 v65, 31, v41
	v_cmp_lt_i32_e32 vcc, -1, v77
	v_bitop3_b32 v41, v41, v65, v132 bitop3:0x1e
	v_min_u32_e32 v58, v58, v60
	v_cndmask_b32_e32 v65, -1, v132, vcc
	v_max_u32_e32 v60, v74, v59
	v_min_u32_e32 v59, v74, v59
	v_ashrrev_i32_e32 v66, 31, v42
	v_bitop3_b32 v42, v42, v66, v132 bitop3:0x1e
	v_max_u32_e32 v74, v50, v51
	v_ashrrev_i32_e32 v66, 31, v54
	v_bitop3_b32 v54, v54, v66, v132 bitop3:0x1e
	v_min_u32_e32 v50, v50, v51
	v_ashrrev_i32_e32 v66, 31, v43
	v_bitop3_b32 v43, v43, v66, v132 bitop3:0x1e
	v_max_u32_e32 v51, v52, v53
	v_ashrrev_i32_e32 v66, 31, v55
	v_bitop3_b32 v55, v55, v66, v132 bitop3:0x1e
	v_min_u32_e32 v52, v52, v53
	v_ashrrev_i32_e32 v66, 31, v44
	v_bitop3_b32 v44, v44, v66, v132 bitop3:0x1e
	v_max_u32_e32 v53, v74, v51
	v_ashrrev_i32_e32 v66, 31, v56
	v_bitop3_b32 v56, v56, v66, v132 bitop3:0x1e
	v_min_u32_e32 v51, v74, v51
	v_ashrrev_i32_e32 v66, 31, v45
	v_cmp_lt_i32_e32 vcc, -1, v57
	v_bitop3_b32 v45, v45, v66, v132 bitop3:0x1e
	v_max_u32_e32 v74, v50, v52
	v_cndmask_b32_e32 v66, -1, v132, vcc
	v_xor_b32_e32 v57, v66, v57
	v_max_u32_e32 v66, v46, v47
	v_min_u32_e32 v46, v46, v47
	v_max_u32_e32 v47, v48, v49
	v_min_u32_e32 v48, v48, v49
	v_max_u32_e32 v49, v66, v47
	v_min_u32_e32 v47, v66, v47
	v_max_u32_e32 v66, v46, v48
	v_min_u32_e32 v46, v46, v48
	v_max_u32_e32 v48, v66, v47
	v_min_u32_e32 v47, v66, v47
	v_max_u32_e32 v66, v34, v35
	v_min_u32_e32 v34, v34, v35
	v_max_u32_e32 v35, v36, v37
	v_min_u32_e32 v36, v36, v37
	v_max_u32_e32 v37, v66, v35
	v_min_u32_e32 v35, v66, v35
	v_max_u32_e32 v66, v34, v36
	v_min_u32_e32 v34, v34, v36
	v_max_u32_e32 v36, v66, v35
	v_min_u32_e32 v35, v66, v35
	v_min_u32_e32 v50, v50, v52
	v_max_u32_e32 v52, v74, v51
	v_min_u32_e32 v51, v74, v51
	v_max_u32_e32 v66, v49, v37
	v_min_u32_e32 v37, v49, v37
	v_max_u32_e32 v49, v47, v35
	v_max_u32_e32 v74, v61, v53
	v_min_u32_e32 v53, v61, v53
	v_max_u32_e32 v61, v59, v51
	v_xor_b32_e32 v63, v63, v75
	v_xor_b32_e32 v64, v64, v76
	v_xor_b32_e32 v65, v65, v77
	v_min_u32_e32 v35, v47, v35
	v_max_u32_e32 v47, v49, v37
	v_min_u32_e32 v37, v49, v37
	v_max_u32_e32 v49, v48, v36
	v_min_u32_e32 v36, v48, v36
	v_max_u32_e32 v48, v46, v34
	v_min_u32_e32 v51, v59, v51
	v_max_u32_e32 v59, v61, v53
	v_min_u32_e32 v53, v61, v53
	v_max_u32_e32 v61, v60, v52
	v_min_u32_e32 v52, v60, v52
	v_max_u32_e32 v60, v58, v50
	v_and_or_b32 v62, v62, s53, v115
	v_and_or_b32 v39, v39, s53, v116
	v_and_or_b32 v63, v63, s53, v117
	v_and_or_b32 v40, v40, s53, v118
	v_and_or_b32 v64, v64, s53, v119
	v_and_or_b32 v41, v41, s53, v120
	v_and_or_b32 v65, v65, s53, v121
	v_min_u32_e32 v34, v46, v34
	v_max_u32_e32 v46, v48, v36
	v_min_u32_e32 v36, v48, v36
	v_min_u32_e32 v50, v58, v50
	v_max_u32_e32 v58, v60, v52
	v_min_u32_e32 v52, v60, v52
	v_max_u32_e32 v48, v49, v47
	v_min_u32_e32 v47, v49, v47
	v_max_u32_e32 v49, v46, v37
	v_min_u32_e32 v37, v46, v37
	v_max_u32_e32 v46, v36, v35
	v_min_u32_e32 v35, v36, v35
	v_max_u32_e32 v36, v38, v39
	v_min_u32_e32 v38, v38, v39
	v_max_u32_e32 v39, v40, v41
	v_min_u32_e32 v40, v40, v41
	v_max_u32_e32 v60, v61, v59
; __device__ __forceinline__ void topk_phase(LAS unsigned char* lds, const bf16_t* qp, const bf16_t* keys, const float* SU, const float* SV, int* sel_e, float* sel_g, float* sel_su, int G, int b) {
;     ...
;             SN_SORT16(T[p]); SN_SORT16(lo16);
; #pragma unroll
;             for (int i = 0; i < 16; ++i) T[p][i] = umax_(T[p][i], lo16[15 - i]);
;             SN_BITONIC16(T[p]);
	v_min_u32_e32 v59, v61, v59
	v_max_u32_e32 v61, v58, v53
	v_min_u32_e32 v53, v58, v53
	v_max_u32_e32 v58, v52, v51
	v_min_u32_e32 v51, v52, v51
	v_max_u32_e32 v52, v62, v63
	v_min_u32_e32 v62, v62, v63
	v_max_u32_e32 v63, v64, v65
	v_min_u32_e32 v64, v64, v65
	v_and_or_b32 v42, v42, s53, v122
	v_and_or_b32 v54, v54, s53, v123
	v_and_or_b32 v43, v43, s53, v124
	v_and_or_b32 v55, v55, s53, v125
	v_and_or_b32 v44, v44, s53, v126
	v_and_or_b32 v56, v56, s53, v127
	v_and_or_b32 v45, v45, s53, v128
	v_and_or_b32 v57, v57, s53, v129
	v_max_u32_e32 v41, v36, v39
	v_min_u32_e32 v36, v36, v39
	v_max_u32_e32 v39, v38, v40
	v_max_u32_e32 v65, v52, v63
	v_min_u32_e32 v52, v52, v63
	v_max_u32_e32 v63, v62, v64
	v_min_u32_e32 v38, v38, v40
	v_max_u32_e32 v40, v39, v36
	v_min_u32_e32 v36, v39, v36
	v_max_u32_e32 v39, v42, v43
	v_min_u32_e32 v42, v42, v43
	v_max_u32_e32 v43, v44, v45
	v_min_u32_e32 v44, v44, v45
	v_min_u32_e32 v62, v62, v64
	v_max_u32_e32 v64, v63, v52
	v_min_u32_e32 v52, v63, v52
	v_max_u32_e32 v63, v54, v55
	v_min_u32_e32 v54, v54, v55
	v_max_u32_e32 v55, v56, v57
	v_min_u32_e32 v56, v56, v57
	v_max_u32_e32 v45, v39, v43
	v_min_u32_e32 v39, v39, v43
	v_max_u32_e32 v43, v42, v44
	v_max_u32_e32 v57, v63, v55
	v_min_u32_e32 v55, v63, v55
	v_max_u32_e32 v63, v54, v56
	v_min_u32_e32 v42, v42, v44
	v_max_u32_e32 v44, v43, v39
	v_min_u32_e32 v39, v43, v39
	v_min_u32_e32 v54, v54, v56
	v_max_u32_e32 v56, v63, v55
	v_min_u32_e32 v55, v63, v55
	v_max_u32_e32 v43, v41, v45
	v_min_u32_e32 v41, v41, v45
	v_max_u32_e32 v45, v36, v39
	v_max_u32_e32 v63, v65, v57
	v_min_u32_e32 v57, v65, v57
	v_max_u32_e32 v65, v52, v55
	v_min_u32_e32 v36, v36, v39
	v_max_u32_e32 v39, v45, v41
	v_min_u32_e32 v41, v45, v41
	v_max_u32_e32 v45, v40, v44
	v_min_u32_e32 v40, v40, v44
	v_max_u32_e32 v44, v38, v42
	v_min_u32_e32 v52, v52, v55
	v_max_u32_e32 v55, v65, v57
	v_min_u32_e32 v57, v65, v57
	v_max_u32_e32 v65, v64, v56
	v_min_u32_e32 v56, v64, v56
	v_max_u32_e32 v64, v62, v54
	v_min_u32_e32 v38, v38, v42
	v_max_u32_e32 v42, v44, v40
	v_min_u32_e32 v54, v62, v54
	v_max_u32_e32 v62, v64, v56
	v_min_u32_e32 v40, v44, v40
	v_max_u32_e32 v44, v45, v39
	v_min_u32_e32 v39, v45, v39
	v_max_u32_e32 v45, v42, v41
	v_min_u32_e32 v41, v42, v41
	v_min_u32_e32 v56, v64, v56
	v_max_u32_e32 v64, v65, v55
	v_min_u32_e32 v55, v65, v55
	v_max_u32_e32 v65, v62, v57
	v_min_u32_e32 v57, v62, v57
	v_max_u32_e32 v42, v40, v36
	v_min_u32_e32 v36, v40, v36
	v_min_u32_e32 v40, v66, v43
	v_max_u32_e32 v67, v37, v41
	v_max_u32_e32 v62, v56, v52
	v_min_u32_e32 v52, v56, v52
	v_min_u32_e32 v56, v74, v63
	v_max_u32_e32 v75, v53, v57
	v_min_u32_e32 v37, v37, v41
	v_max_u32_e32 v41, v67, v40
	v_min_u32_e32 v40, v67, v40
	v_max_u32_e32 v67, v47, v39
	v_min_u32_e32 v39, v47, v39
	v_max_u32_e32 v47, v35, v36
	v_min_u32_e32 v53, v53, v57
	v_max_u32_e32 v57, v75, v56
	v_min_u32_e32 v56, v75, v56
	v_max_u32_e32 v75, v59, v55
	v_min_u32_e32 v55, v59, v55
	v_max_u32_e32 v59, v51, v52
	v_min_u32_e32 v35, v35, v36
	v_max_u32_e32 v36, v47, v39
	v_min_u32_e32 v39, v47, v39
	v_min_u32_e32 v51, v51, v52
	v_max_u32_e32 v52, v59, v55
	v_min_u32_e32 v55, v59, v55
	v_max_u32_e32 v47, v67, v41
	v_min_u32_e32 v41, v67, v41
	v_max_u32_e32 v67, v36, v40
	v_min_u32_e32 v36, v36, v40
	v_max_u32_e32 v40, v39, v37
	v_min_u32_e32 v37, v39, v37
	v_max_u32_e32 v39, v48, v44
	v_min_u32_e32 v44, v48, v44
	v_max_u32_e32 v48, v46, v42
	v_max_u32_e32 v59, v75, v57
	v_min_u32_e32 v57, v75, v57
	v_max_u32_e32 v75, v52, v56
	v_min_u32_e32 v52, v52, v56
	v_max_u32_e32 v56, v55, v53
	v_min_u32_e32 v53, v55, v53
	v_max_u32_e32 v55, v60, v64
	v_min_u32_e32 v60, v60, v64
	v_max_u32_e32 v64, v58, v62
	v_min_u32_e32 v42, v46, v42
	v_max_u32_e32 v46, v48, v44
	v_min_u32_e32 v44, v48, v44
	v_max_u32_e32 v48, v49, v45
	v_min_u32_e32 v45, v49, v45
	v_max_u32_e32 v49, v34, v38
	v_min_u32_e32 v58, v58, v62
	v_max_u32_e32 v62, v64, v60
	v_min_u32_e32 v60, v64, v60
	v_max_u32_e32 v64, v61, v65
	v_min_u32_e32 v61, v61, v65
	v_max_u32_e32 v65, v50, v54
	v_min_u32_e32 v34, v34, v38
	v_max_u32_e32 v38, v49, v45
	v_min_u32_e32 v45, v49, v45
	v_min_u32_e32 v50, v50, v54
	v_max_u32_e32 v54, v65, v61
	v_min_u32_e32 v61, v65, v61
	v_max_u32_e32 v49, v48, v46
	v_min_u32_e32 v46, v48, v46
	v_max_u32_e32 v48, v38, v44
	v_min_u32_e32 v38, v38, v44
	v_max_u32_e32 v44, v45, v42
	v_min_u32_e32 v42, v45, v42
	v_max_u32_e32 v65, v64, v62
	v_min_u32_e32 v62, v64, v62
	v_max_u32_e32 v64, v54, v60
	v_min_u32_e32 v54, v54, v60
	v_max_u32_e32 v60, v61, v58
	v_min_u32_e32 v58, v61, v58
	v_min_u32_e32 v45, v39, v47
	v_min_u32_e32 v68, v49, v41
	v_min_u32_e32 v69, v46, v67
	v_min_u32_e32 v70, v48, v36
	v_min_u32_e32 v71, v38, v40
	v_min_u32_e32 v72, v44, v37
	v_min_u32_e32 v73, v42, v35
	v_min_u32_e32 v61, v55, v59
	v_min_u32_e32 v76, v65, v57
	v_min_u32_e32 v77, v62, v75
	v_min_u32_e32 v134, v64, v52
	v_min_u32_e32 v135, v54, v56
	v_min_u32_e32 v136, v60, v53
	v_min_u32_e32 v137, v58, v51
	v_max3_u32 v43, v66, v43, v50
	v_max3_u32 v39, v39, v47, v137
	v_max3_u32 v45, v45, v58, v51
	v_max3_u32 v41, v49, v41, v136
	v_max3_u32 v47, v68, v60, v53
	v_max3_u32 v46, v46, v67, v135
	v_max3_u32 v49, v69, v54, v56
	v_max3_u32 v36, v48, v36, v134
	v_max3_u32 v48, v70, v64, v52
	v_max3_u32 v38, v38, v40, v77
	v_max3_u32 v40, v71, v62, v75
	v_max3_u32 v37, v44, v37, v76
	v_max3_u32 v44, v72, v65, v57
	v_max3_u32 v35, v42, v35, v61
	v_max3_u32 v42, v73, v55, v59
	v_max3_u32 v34, v34, v74, v63
	v_max_u32_e32 v50, v43, v48
	v_min_u32_e32 v43, v43, v48
	v_max_u32_e32 v48, v39, v38
	v_min_u32_e32 v38, v39, v38
	v_max_u32_e32 v39, v45, v40
	v_min_u32_e32 v40, v45, v40
	v_max_u32_e32 v45, v41, v37
; __device__ __forceinline__ void topk_phase(LAS unsigned char* lds, const bf16_t* qp, const bf16_t* keys, const float* SU, const float* SV, int* sel_e, float* sel_g, float* sel_su, int G, int b) {
;     ...
;             for (int ks = 0; ks < 4; ++ks) bq[ks] = *(const bf16x8*)(qp + (size_t)tok * D_ + h * 256 + p * 128 + ks * 32 + fq * 8);
;     ...
;             for (int i = 0; i < 16; ++i) T[p][i] = umax_(T[p][i], lo16[15 - i]);
;             SN_BITONIC16(T[p]);
;             TOPK_XMERGE(T[p], 16); TOPK_XMERGE(T[p], 32);
	v_min_u32_e32 v37, v41, v37
	v_max_u32_e32 v41, v47, v44
	v_min_u32_e32 v44, v47, v44
	v_max_u32_e32 v47, v46, v35
	v_min_u32_e32 v35, v46, v35
	v_max_u32_e32 v46, v49, v42
	v_min_u32_e32 v42, v49, v42
	v_max_u32_e32 v49, v36, v34
	v_min_u32_e32 v34, v36, v34
	v_max_u32_e32 v36, v50, v41
	v_min_u32_e32 v41, v50, v41
	v_max_u32_e32 v50, v48, v47
	v_min_u32_e32 v47, v48, v47
	v_max_u32_e32 v48, v39, v46
	v_min_u32_e32 v39, v39, v46
	v_max_u32_e32 v46, v45, v49
	v_min_u32_e32 v45, v45, v49
	v_max_u32_e32 v49, v43, v44
	v_min_u32_e32 v43, v43, v44
	v_max_u32_e32 v44, v38, v35
	v_min_u32_e32 v35, v38, v35
	v_max_u32_e32 v38, v40, v42
	v_min_u32_e32 v40, v40, v42
	v_max_u32_e32 v42, v37, v34
	v_min_u32_e32 v34, v37, v34
	v_max_u32_e32 v37, v36, v48
	v_min_u32_e32 v36, v36, v48
	v_max_u32_e32 v48, v50, v46
	v_min_u32_e32 v46, v50, v46
	v_max_u32_e32 v50, v41, v39
	v_min_u32_e32 v39, v41, v39
	v_max_u32_e32 v41, v47, v45
	v_min_u32_e32 v45, v47, v45
	v_max_u32_e32 v47, v49, v38
	v_min_u32_e32 v38, v49, v38
	v_max_u32_e32 v49, v44, v42
	v_min_u32_e32 v42, v44, v42
	v_max_u32_e32 v44, v43, v40
	v_min_u32_e32 v40, v43, v40
	v_max_u32_e32 v43, v35, v34
	v_min_u32_e32 v34, v35, v34
	v_max_u32_e32 v35, v37, v48
	v_min_u32_e32 v37, v37, v48
	v_max_u32_e32 v48, v36, v46
	v_min_u32_e32 v36, v36, v46
	v_max_u32_e32 v46, v50, v41
	v_min_u32_e32 v41, v50, v41
	v_max_u32_e32 v50, v39, v45
	v_min_u32_e32 v39, v39, v45
	v_max_u32_e32 v45, v47, v49
	v_min_u32_e32 v47, v47, v49
	v_max_u32_e32 v49, v38, v42
	v_min_u32_e32 v38, v38, v42
	v_max_u32_e32 v42, v44, v43
	v_min_u32_e32 v43, v44, v43
	v_max_u32_e32 v44, v40, v34
	v_min_u32_e32 v34, v40, v34
	v_mov_b32_e32 v40, v35
	v_mov_b32_e32 v51, v37
	v_mov_b32_e32 v52, v48
	v_mov_b32_e32 v53, v36
	v_mov_b32_e32 v54, v46
	v_mov_b32_e32 v55, v41
	v_mov_b32_e32 v56, v50
	v_mov_b32_e32 v57, v39
	v_mov_b32_e32 v58, v45
	v_mov_b32_e32 v59, v47
	v_mov_b32_e32 v60, v49
	v_mov_b32_e32 v61, v38
	v_mov_b32_e32 v62, v42
	v_mov_b32_e32 v63, v43
	v_mov_b32_e32 v64, v44
	v_mov_b32_e32 v65, v34
	v_permlane16_swap_b32_e32 v35, v40
	v_permlane16_swap_b32_e32 v37, v51
	v_permlane16_swap_b32_e32 v48, v52
	v_permlane16_swap_b32_e32 v36, v53
	v_permlane16_swap_b32_e32 v46, v54
	v_permlane16_swap_b32_e32 v41, v55
	v_permlane16_swap_b32_e32 v50, v56
	v_permlane16_swap_b32_e32 v39, v57
	v_permlane16_swap_b32_e32 v45, v58
	v_permlane16_swap_b32_e32 v47, v59
	v_permlane16_swap_b32_e32 v49, v60
	v_permlane16_swap_b32_e32 v38, v61
	v_permlane16_swap_b32_e32 v42, v62
	v_permlane16_swap_b32_e32 v43, v63
	v_permlane16_swap_b32_e32 v44, v64
	v_permlane16_swap_b32_e32 v34, v65
	v_max_u32_e32 v35, v35, v65
	v_max_u32_e32 v37, v37, v64
	v_max_u32_e32 v48, v48, v63
	v_max_u32_e32 v36, v36, v62
	v_max_u32_e32 v46, v46, v61
	v_max_u32_e32 v41, v41, v60
	v_max_u32_e32 v50, v50, v59
	v_max_u32_e32 v39, v39, v58
	v_max_u32_e32 v45, v45, v57
	v_max_u32_e32 v47, v47, v56
	v_max_u32_e32 v49, v49, v55
	v_max_u32_e32 v38, v38, v54
	v_max_u32_e32 v42, v42, v53
	v_max_u32_e32 v43, v43, v52
	v_max_u32_e32 v44, v44, v51
	v_max_u32_e32 v34, v34, v40
	v_max_u32_e32 v40, v35, v45
	v_min_u32_e32 v35, v35, v45
	v_max_u32_e32 v45, v37, v47
	v_min_u32_e32 v37, v37, v47
	v_max_u32_e32 v47, v48, v49
	v_min_u32_e32 v48, v48, v49
	v_max_u32_e32 v49, v36, v38
	v_min_u32_e32 v36, v36, v38
	v_max_u32_e32 v38, v46, v42
	v_min_u32_e32 v42, v46, v42
	v_max_u32_e32 v46, v41, v43
	v_min_u32_e32 v41, v41, v43
	v_max_u32_e32 v43, v50, v44
	v_min_u32_e32 v44, v50, v44
	v_max_u32_e32 v50, v39, v34
	v_min_u32_e32 v34, v39, v34
	v_max_u32_e32 v39, v40, v38
	v_min_u32_e32 v38, v40, v38
	v_max_u32_e32 v40, v45, v46
	v_min_u32_e32 v45, v45, v46
	v_max_u32_e32 v46, v47, v43
	v_min_u32_e32 v43, v47, v43
	v_max_u32_e32 v47, v49, v50
	v_min_u32_e32 v49, v49, v50
	v_max_u32_e32 v50, v35, v42
	v_min_u32_e32 v35, v35, v42
	v_max_u32_e32 v42, v37, v41
	v_min_u32_e32 v37, v37, v41
	v_max_u32_e32 v41, v48, v44
	v_min_u32_e32 v44, v48, v44
	v_max_u32_e32 v48, v36, v34
	v_min_u32_e32 v34, v36, v34
	v_max_u32_e32 v36, v39, v46
	v_min_u32_e32 v39, v39, v46
	v_max_u32_e32 v46, v40, v47
	v_min_u32_e32 v40, v40, v47
	v_max_u32_e32 v47, v38, v43
	v_min_u32_e32 v38, v38, v43
	v_max_u32_e32 v43, v45, v49
	v_min_u32_e32 v45, v45, v49
	v_max_u32_e32 v49, v50, v41
	v_min_u32_e32 v41, v50, v41
	v_max_u32_e32 v50, v42, v48
	v_min_u32_e32 v42, v42, v48
	v_max_u32_e32 v48, v35, v44
	v_min_u32_e32 v35, v35, v44
	v_max_u32_e32 v44, v37, v34
	v_min_u32_e32 v34, v37, v34
	v_max_u32_e32 v70, v36, v46
	v_min_u32_e32 v71, v36, v46
	v_max_u32_e32 v72, v39, v40
	v_min_u32_e32 v73, v39, v40
	v_max_u32_e32 v74, v47, v43
	v_min_u32_e32 v75, v47, v43
	v_max_u32_e32 v76, v38, v45
	v_min_u32_e32 v77, v38, v45
	v_max_u32_e32 v134, v49, v50
	v_min_u32_e32 v135, v49, v50
	v_max_u32_e32 v136, v41, v42
	v_min_u32_e32 v137, v41, v42
	v_max_u32_e32 v138, v48, v44
	v_min_u32_e32 v139, v48, v44
	v_max_u32_e32 v140, v35, v34
	v_min_u32_e32 v141, v35, v34
	global_load_dwordx4 v[46:49], v[96:97], off offset:256
	global_load_dwordx4 v[42:45], v[96:97], off offset:320
	global_load_dwordx4 v[38:41], v[96:97], off offset:384
	global_load_dwordx4 v[34:37], v[96:97], off offset:448
	ds_read_b128 v[50:53], v131 offset:34816
	ds_read_b128 v[54:57], v131 offset:34880
	s_waitcnt vmcnt(3) lgkmcnt(1)
	v_mfma_f32_16x16x32_bf16 v[50:53], v[50:53], v[46:49], 0
	ds_read_b128 v[58:61], v131 offset:39232
	ds_read_b128 v[62:65], v131 offset:43584
	ds_read_b128 v[66:69], v131 offset:47936
	s_waitcnt vmcnt(2) lgkmcnt(3)
	v_mfma_f32_16x16x32_bf16 v[50:53], v[54:57], v[42:45], v[50:53]
	ds_read_b128 v[54:57], v131 offset:34944
	ds_read_b128 v[158:161], v131 offset:52288
	ds_read_b128 v[162:165], v131 offset:56640
	s_waitcnt vmcnt(1) lgkmcnt(2)
; #define LAS __attribute__((address_space(3)))
; __device__ __forceinline__ f32x4 mfma16(bf16x8 a, bf16x8 b, f32x4 c) { return __builtin_amdgcn_mfma_f32_16x16x32_bf16(a, b, c, 0, 0, 0); }
; __device__ __forceinline__ void topk_phase(LAS unsigned char* lds, const bf16_t* qp, const bf16_t* keys, const float* SU, const float* SV, int* sel_e, float* sel_g, float* sel_su, int G, int b) {
;     ...
;             for (int ks = 0; ks < 4; ++ks) bq[ks] = *(const bf16x8*)(qp + (size_t)tok * D_ + h * 256 + p * 128 + ks * 32 + fq * 8);
;             const LAS bf16_t* kb = KL + p * 128 * 136;
; #pragma unroll
;             for (int mt = 0; mt < 8; ++mt)
; #pragma unroll
;                 for (int ks = 0; ks < 4; ++ks) { const bf16x8 a = *(const LAS bf16x8*)(kb + (mt * 16 + fr) * 136 + ks * 32 + fq * 8); acc[mt] = mfma16(a, bq[ks], acc[mt]); }
	v_mfma_f32_16x16x32_bf16 v[50:53], v[54:57], v[38:41], v[50:53]
	ds_read_b128 v[54:57], v131 offset:35008
	ds_read_b128 v[166:169], v131 offset:60992
	v_mov_b32_e32 v142, v70
	s_waitcnt vmcnt(0) lgkmcnt(1)
	v_mfma_f32_16x16x32_bf16 v[50:53], v[54:57], v[34:37], v[50:53]
	ds_read_b128 v[54:57], v131 offset:39168
	v_mov_b32_e32 v143, v71
	v_mov_b32_e32 v144, v72
	s_waitcnt lgkmcnt(0)
	v_mfma_f32_16x16x32_bf16 v[54:57], v[54:57], v[46:49], 0
	s_nop 2
	v_mov_b32_e32 v145, v73
	v_mov_b32_e32 v146, v74
	v_mfma_f32_16x16x32_bf16 v[54:57], v[58:61], v[42:45], v[54:57]
	ds_read_b128 v[58:61], v131 offset:39296
	v_mov_b32_e32 v147, v75
	v_mov_b32_e32 v148, v76
	s_waitcnt lgkmcnt(0)
	v_mfma_f32_16x16x32_bf16 v[54:57], v[58:61], v[38:41], v[54:57]
	ds_read_b128 v[58:61], v131 offset:39360
	v_mov_b32_e32 v149, v77
	v_mov_b32_e32 v150, v134
	s_waitcnt lgkmcnt(0)
	v_mfma_f32_16x16x32_bf16 v[54:57], v[58:61], v[34:37], v[54:57]
	ds_read_b128 v[58:61], v131 offset:43520
	v_mov_b32_e32 v151, v135
	v_mov_b32_e32 v152, v136
	s_waitcnt lgkmcnt(0)
	v_mfma_f32_16x16x32_bf16 v[58:61], v[58:61], v[46:49], 0
	v_mov_b32_e32 v153, v137
	v_mov_b32_e32 v154, v138
	v_mov_b32_e32 v155, v139
	v_mfma_f32_16x16x32_bf16 v[58:61], v[62:65], v[42:45], v[58:61]
	ds_read_b128 v[62:65], v131 offset:43648
	v_mov_b32_e32 v156, v140
	v_mov_b32_e32 v157, v141
	s_waitcnt lgkmcnt(0)
	v_mfma_f32_16x16x32_bf16 v[58:61], v[62:65], v[38:41], v[58:61]
	ds_read_b128 v[62:65], v131 offset:43712
	v_permlane32_swap_b32_e32 v70, v142
	s_waitcnt lgkmcnt(0)
	v_mfma_f32_16x16x32_bf16 v[58:61], v[62:65], v[34:37], v[58:61]
	ds_read_b128 v[62:65], v131 offset:47872
	v_permlane32_swap_b32_e32 v71, v143
	s_waitcnt lgkmcnt(0)
	v_mfma_f32_16x16x32_bf16 v[62:65], v[62:65], v[46:49], 0
	v_permlane32_swap_b32_e32 v72, v144
	v_permlane32_swap_b32_e32 v73, v145
	v_mfma_f32_16x16x32_bf16 v[62:65], v[66:69], v[42:45], v[62:65]
	ds_read_b128 v[66:69], v131 offset:48000
	v_permlane32_swap_b32_e32 v74, v146
	s_waitcnt lgkmcnt(0)
	v_mfma_f32_16x16x32_bf16 v[62:65], v[66:69], v[38:41], v[62:65]
	ds_read_b128 v[66:69], v131 offset:48064
	v_permlane32_swap_b32_e32 v75, v147
	s_waitcnt lgkmcnt(0)
	v_mfma_f32_16x16x32_bf16 v[62:65], v[66:69], v[34:37], v[62:65]
	ds_read_b128 v[66:69], v131 offset:52224
	v_permlane32_swap_b32_e32 v76, v148
	s_waitcnt lgkmcnt(0)
	v_mfma_f32_16x16x32_bf16 v[66:69], v[66:69], v[46:49], 0
	v_permlane32_swap_b32_e32 v77, v149
	v_permlane32_swap_b32_e32 v134, v150
	v_mfma_f32_16x16x32_bf16 v[66:69], v[158:161], v[42:45], v[66:69]
	ds_read_b128 v[158:161], v131 offset:52352
	v_permlane32_swap_b32_e32 v135, v151
	s_waitcnt lgkmcnt(0)
	v_mfma_f32_16x16x32_bf16 v[66:69], v[158:161], v[38:41], v[66:69]
	ds_read_b128 v[158:161], v131 offset:52416
	v_permlane32_swap_b32_e32 v136, v152
	s_waitcnt lgkmcnt(0)
	v_mfma_f32_16x16x32_bf16 v[66:69], v[158:161], v[34:37], v[66:69]
	ds_read_b128 v[158:161], v131 offset:56576
	v_permlane32_swap_b32_e32 v137, v153
	s_waitcnt lgkmcnt(0)
	v_mfma_f32_16x16x32_bf16 v[158:161], v[158:161], v[46:49], 0
	v_permlane32_swap_b32_e32 v138, v154
	v_permlane32_swap_b32_e32 v139, v155
	v_mfma_f32_16x16x32_bf16 v[158:161], v[162:165], v[42:45], v[158:161]
	ds_read_b128 v[162:165], v131 offset:56704
	v_permlane32_swap_b32_e32 v140, v156
	s_waitcnt lgkmcnt(0)
	v_mfma_f32_16x16x32_bf16 v[158:161], v[162:165], v[38:41], v[158:161]
	ds_read_b128 v[162:165], v131 offset:56768
	v_permlane32_swap_b32_e32 v141, v157
	s_waitcnt lgkmcnt(0)
	v_mfma_f32_16x16x32_bf16 v[158:161], v[162:165], v[34:37], v[158:161]
	ds_read_b128 v[162:165], v131 offset:60928
	s_waitcnt lgkmcnt(0)
	v_mfma_f32_16x16x32_bf16 v[162:165], v[162:165], v[46:49], 0
	v_mfma_f32_16x16x32_bf16 v[162:165], v[166:169], v[42:45], v[162:165]
	ds_read_b128 v[166:169], v131 offset:61056
	s_waitcnt lgkmcnt(0)
	v_mfma_f32_16x16x32_bf16 v[162:165], v[166:169], v[38:41], v[162:165]
	ds_read_b128 v[166:169], v131 offset:61120
	s_waitcnt lgkmcnt(0)
	v_mfma_f32_16x16x32_bf16 v[162:165], v[166:169], v[34:37], v[162:165]
	ds_read_b128 v[166:169], v131 offset:65280
	s_waitcnt lgkmcnt(0)
	v_mfma_f32_16x16x32_bf16 v[46:49], v[166:169], v[46:49], 0
	ds_read_b128 v[166:169], v131 offset:65344
	s_waitcnt lgkmcnt(0)
	v_mfma_f32_16x16x32_bf16 v[42:45], v[166:169], v[42:45], v[46:49]
	s_nop 4
	ds_read_b128 v[46:49], v131 offset:65408
	s_waitcnt lgkmcnt(0)
	v_mfma_f32_16x16x32_bf16 v[38:41], v[46:49], v[38:41], v[42:45]
	s_nop 2
	ds_read_b128 v[42:45], v131 offset:65472
	s_waitcnt lgkmcnt(0)
; __device__ __forceinline__ unsigned mono(float f) { const unsigned u = __float_as_uint(f); return (u & 0x80000000u) ? ~u : (u ^ 0x80000000u); }
; __device__ __forceinline__ void topk_phase(LAS unsigned char* lds, const bf16_t* qp, const bf16_t* keys, const float* SU, const float* SV, int* sel_e, float* sel_g, float* sel_su, int G, int b) {
;     ...
;             unsigned lo16[16];
; #pragma unroll
;             for (int mt = 0; mt < 4; ++mt)
; #pragma unroll
;                 for (int r = 0; r < 4; ++r) {
;                     T[p][mt * 4 + r] = (mono(acc[mt][r]) & ~127u) | (unsigned)(127 - (mt * 16 + fq * 4 + r));
;                     lo16[mt * 4 + r] = (mono(acc[mt + 4][r]) & ~127u) | (unsigned)(127 - ((mt + 4) * 16 + fq * 4 + r));
;                 }
;             SN_SORT16(T[p]); SN_SORT16(lo16);
	v_mfma_f32_16x16x32_bf16 v[34:37], v[42:45], v[34:37], v[38:41]
	s_nop 2
	v_ashrrev_i32_e32 v38, 31, v50
	v_bitop3_b32 v38, v50, v38, v132 bitop3:0x1e
	v_and_or_b32 v38, v38, s53, v98
	v_ashrrev_i32_e32 v39, 31, v66
	v_bitop3_b32 v39, v66, v39, v132 bitop3:0x1e
	v_and_or_b32 v39, v39, s53, v99
	v_ashrrev_i32_e32 v40, 31, v51
	v_bitop3_b32 v40, v51, v40, v132 bitop3:0x1e
	v_and_or_b32 v40, v40, s53, v100
	v_ashrrev_i32_e32 v41, 31, v67
	v_bitop3_b32 v41, v67, v41, v132 bitop3:0x1e
	v_and_or_b32 v41, v41, s53, v101
	v_ashrrev_i32_e32 v42, 31, v52
	v_bitop3_b32 v42, v52, v42, v132 bitop3:0x1e
	v_and_or_b32 v42, v42, s53, v102
	v_ashrrev_i32_e32 v43, 31, v68
	v_bitop3_b32 v43, v68, v43, v132 bitop3:0x1e
	v_and_or_b32 v43, v43, s53, v103
	v_ashrrev_i32_e32 v44, 31, v53
	v_bitop3_b32 v44, v53, v44, v132 bitop3:0x1e
	v_and_or_b32 v44, v44, s53, v104
	v_ashrrev_i32_e32 v45, 31, v69
	v_bitop3_b32 v45, v69, v45, v132 bitop3:0x1e
	v_and_or_b32 v45, v45, s53, v105
	v_ashrrev_i32_e32 v46, 31, v54
	v_bitop3_b32 v46, v54, v46, v132 bitop3:0x1e
	v_and_or_b32 v46, v46, s53, v106
	v_ashrrev_i32_e32 v47, 31, v158
	v_bitop3_b32 v47, v158, v47, v132 bitop3:0x1e
	v_and_or_b32 v47, v47, s53, v107
	v_ashrrev_i32_e32 v48, 31, v55
	v_bitop3_b32 v48, v55, v48, v132 bitop3:0x1e
	v_and_or_b32 v48, v48, s53, v108
	v_ashrrev_i32_e32 v49, 31, v159
	v_bitop3_b32 v49, v159, v49, v132 bitop3:0x1e
	v_and_or_b32 v49, v49, s53, v109
	v_ashrrev_i32_e32 v50, 31, v56
	v_bitop3_b32 v50, v56, v50, v132 bitop3:0x1e
	v_and_or_b32 v50, v50, s53, v110
	v_ashrrev_i32_e32 v51, 31, v160
	v_bitop3_b32 v51, v160, v51, v132 bitop3:0x1e
	v_max_u32_e32 v160, v39, v41
	v_ashrrev_i32_e32 v52, 31, v57
	v_bitop3_b32 v52, v57, v52, v132 bitop3:0x1e
	v_min_u32_e32 v39, v39, v41
	v_ashrrev_i32_e32 v53, 31, v161
	v_bitop3_b32 v53, v161, v53, v132 bitop3:0x1e
	v_max_u32_e32 v41, v43, v45
	v_ashrrev_i32_e32 v54, 31, v58
	v_cmp_lt_i32_e32 vcc, -1, v162
	v_bitop3_b32 v54, v58, v54, v132 bitop3:0x1e
	v_min_u32_e32 v43, v43, v45
	v_cndmask_b32_e32 v55, -1, v132, vcc
	v_and_or_b32 v51, v51, s53, v111
	v_and_or_b32 v52, v52, s53, v112
	v_ashrrev_i32_e32 v56, 31, v59
	v_cmp_lt_i32_e32 vcc, -1, v163
	v_bitop3_b32 v56, v59, v56, v132 bitop3:0x1e
	v_and_or_b32 v53, v53, s53, v113
	v_cndmask_b32_e32 v57, -1, v132, vcc
	v_max_u32_e32 v45, v160, v41
	v_min_u32_e32 v41, v160, v41
	v_ashrrev_i32_e32 v58, 31, v60
	v_cmp_lt_i32_e32 vcc, -1, v164
	v_bitop3_b32 v58, v60, v58, v132 bitop3:0x1e
	v_max_u32_e32 v160, v39, v43
	v_cndmask_b32_e32 v59, -1, v132, vcc
	v_min_u32_e32 v39, v39, v43
	v_max_u32_e32 v43, v160, v41
	v_ashrrev_i32_e32 v60, 31, v61
	v_cmp_lt_i32_e32 vcc, -1, v165
	v_bitop3_b32 v60, v61, v60, v132 bitop3:0x1e
	v_min_u32_e32 v41, v160, v41
	v_cndmask_b32_e32 v61, -1, v132, vcc
	v_max_u32_e32 v160, v47, v49
	v_min_u32_e32 v47, v47, v49
	v_ashrrev_i32_e32 v66, 31, v62
	v_bitop3_b32 v62, v62, v66, v132 bitop3:0x1e
	v_max_u32_e32 v49, v51, v53
	v_ashrrev_i32_e32 v66, 31, v34
	v_bitop3_b32 v34, v34, v66, v132 bitop3:0x1e
	v_min_u32_e32 v51, v51, v53
	v_ashrrev_i32_e32 v66, 31, v63
	v_bitop3_b32 v63, v63, v66, v132 bitop3:0x1e
	v_max_u32_e32 v53, v160, v49
	v_ashrrev_i32_e32 v66, 31, v35
	v_bitop3_b32 v35, v35, v66, v132 bitop3:0x1e
	v_min_u32_e32 v49, v160, v49
	v_ashrrev_i32_e32 v66, 31, v64
	v_bitop3_b32 v64, v64, v66, v132 bitop3:0x1e
	v_max_u32_e32 v160, v47, v51
	v_ashrrev_i32_e32 v66, 31, v36
	v_bitop3_b32 v36, v36, v66, v132 bitop3:0x1e
	v_min_u32_e32 v47, v47, v51
	v_ashrrev_i32_e32 v66, 31, v65
	v_cmp_lt_i32_e32 vcc, -1, v37
	v_bitop3_b32 v65, v65, v66, v132 bitop3:0x1e
	v_max_u32_e32 v51, v160, v49
	v_cndmask_b32_e32 v66, -1, v132, vcc
	v_xor_b32_e32 v37, v66, v37
	v_max_u32_e32 v66, v38, v40
	v_min_u32_e32 v38, v38, v40
	v_max_u32_e32 v40, v42, v44
	v_min_u32_e32 v42, v42, v44
	v_max_u32_e32 v44, v66, v40
	v_min_u32_e32 v40, v66, v40
	v_max_u32_e32 v66, v38, v42
	v_min_u32_e32 v38, v38, v42
	v_max_u32_e32 v42, v66, v40
	v_min_u32_e32 v40, v66, v40
	v_max_u32_e32 v66, v46, v48
	v_min_u32_e32 v46, v46, v48
	v_max_u32_e32 v48, v50, v52
	v_min_u32_e32 v50, v50, v52
	v_max_u32_e32 v52, v66, v48
	v_min_u32_e32 v48, v66, v48
	v_max_u32_e32 v66, v46, v50
	v_min_u32_e32 v46, v46, v50
	v_max_u32_e32 v50, v66, v48
	v_min_u32_e32 v48, v66, v48
	v_min_u32_e32 v49, v160, v49
	v_max_u32_e32 v66, v44, v52
	v_min_u32_e32 v44, v44, v52
	v_max_u32_e32 v52, v40, v48
	v_max_u32_e32 v160, v45, v53
	v_min_u32_e32 v45, v45, v53
	v_max_u32_e32 v53, v41, v49
	v_xor_b32_e32 v55, v55, v162
	v_xor_b32_e32 v57, v57, v163
	v_xor_b32_e32 v59, v59, v164
	v_xor_b32_e32 v61, v61, v165
	v_min_u32_e32 v40, v40, v48
	v_max_u32_e32 v48, v52, v44
	v_min_u32_e32 v44, v52, v44
	v_max_u32_e32 v52, v42, v50
	v_min_u32_e32 v42, v42, v50
	v_max_u32_e32 v50, v38, v46
	v_min_u32_e32 v41, v41, v49
	v_max_u32_e32 v49, v53, v45
	v_min_u32_e32 v45, v53, v45
	v_max_u32_e32 v53, v43, v51
	v_min_u32_e32 v43, v43, v51
	v_max_u32_e32 v51, v39, v47
	v_and_or_b32 v54, v54, s53, v114
	v_and_or_b32 v55, v55, s53, v115
	v_and_or_b32 v56, v56, s53, v116
	v_and_or_b32 v57, v57, s53, v117
	v_and_or_b32 v58, v58, s53, v118
	v_and_or_b32 v59, v59, s53, v119
	v_and_or_b32 v60, v60, s53, v120
	v_and_or_b32 v61, v61, s53, v121
	v_min_u32_e32 v38, v38, v46
	v_max_u32_e32 v46, v50, v42
	v_min_u32_e32 v42, v50, v42
	v_min_u32_e32 v39, v39, v47
	v_max_u32_e32 v47, v51, v43
	v_min_u32_e32 v43, v51, v43
	v_max_u32_e32 v50, v52, v48
	v_min_u32_e32 v48, v52, v48
	v_max_u32_e32 v52, v46, v44
	v_min_u32_e32 v44, v46, v44
	v_max_u32_e32 v46, v42, v40
	v_min_u32_e32 v40, v42, v40
	v_max_u32_e32 v42, v54, v56
	v_min_u32_e32 v54, v54, v56
	v_max_u32_e32 v56, v58, v60
; __device__ __forceinline__ void topk_phase(LAS unsigned char* lds, const bf16_t* qp, const bf16_t* keys, const float* SU, const float* SV, int* sel_e, float* sel_g, float* sel_su, int G, int b) {
;     ...
;             SN_SORT16(T[p]); SN_SORT16(lo16);
; #pragma unroll
;             for (int i = 0; i < 16; ++i) T[p][i] = umax_(T[p][i], lo16[15 - i]);
;             SN_BITONIC16(T[p]);
	v_min_u32_e32 v58, v58, v60
	v_max_u32_e32 v51, v53, v49
	v_min_u32_e32 v49, v53, v49
	v_max_u32_e32 v53, v47, v45
	v_min_u32_e32 v45, v47, v45
	v_max_u32_e32 v47, v43, v41
	v_min_u32_e32 v41, v43, v41
	v_max_u32_e32 v43, v55, v57
	v_min_u32_e32 v55, v55, v57
	v_max_u32_e32 v57, v59, v61
	v_min_u32_e32 v59, v59, v61
	v_and_or_b32 v62, v62, s53, v122
	v_and_or_b32 v34, v34, s53, v123
	v_and_or_b32 v63, v63, s53, v124
	v_and_or_b32 v35, v35, s53, v125
	v_and_or_b32 v64, v64, s53, v126
	v_and_or_b32 v36, v36, s53, v127
	v_and_or_b32 v65, v65, s53, v128
	v_and_or_b32 v37, v37, s53, v129
	v_max_u32_e32 v60, v42, v56
	v_min_u32_e32 v42, v42, v56
	v_max_u32_e32 v56, v54, v58
	v_max_u32_e32 v61, v43, v57
	v_min_u32_e32 v43, v43, v57
	v_max_u32_e32 v57, v55, v59
	v_min_u32_e32 v54, v54, v58
	v_max_u32_e32 v58, v56, v42
	v_min_u32_e32 v42, v56, v42
	v_max_u32_e32 v56, v62, v63
	v_min_u32_e32 v62, v62, v63
	v_max_u32_e32 v63, v64, v65
	v_min_u32_e32 v64, v64, v65
	v_min_u32_e32 v55, v55, v59
	v_max_u32_e32 v59, v57, v43
	v_min_u32_e32 v43, v57, v43
	v_max_u32_e32 v57, v34, v35
	v_min_u32_e32 v34, v34, v35
	v_max_u32_e32 v35, v36, v37
	v_min_u32_e32 v36, v36, v37
	v_max_u32_e32 v65, v56, v63
	v_min_u32_e32 v56, v56, v63
	v_max_u32_e32 v63, v62, v64
	v_max_u32_e32 v37, v57, v35
	v_min_u32_e32 v35, v57, v35
	v_max_u32_e32 v57, v34, v36
	v_min_u32_e32 v62, v62, v64
	v_max_u32_e32 v64, v63, v56
	v_min_u32_e32 v56, v63, v56
	v_min_u32_e32 v34, v34, v36
	v_max_u32_e32 v36, v57, v35
	v_min_u32_e32 v35, v57, v35
	v_max_u32_e32 v63, v60, v65
	v_min_u32_e32 v60, v60, v65
	v_max_u32_e32 v65, v42, v56
	v_max_u32_e32 v57, v61, v37
	v_min_u32_e32 v37, v61, v37
	v_max_u32_e32 v61, v43, v35
	v_min_u32_e32 v42, v42, v56
	v_max_u32_e32 v56, v65, v60
	v_min_u32_e32 v60, v65, v60
	v_max_u32_e32 v65, v58, v64
	v_min_u32_e32 v58, v58, v64
	v_max_u32_e32 v64, v54, v62
	v_min_u32_e32 v35, v43, v35
	v_max_u32_e32 v43, v61, v37
	v_min_u32_e32 v37, v61, v37
	v_max_u32_e32 v61, v59, v36
	v_min_u32_e32 v36, v59, v36
	v_max_u32_e32 v59, v55, v34
	v_min_u32_e32 v54, v54, v62
	v_max_u32_e32 v62, v64, v58
	v_min_u32_e32 v34, v55, v34
	v_max_u32_e32 v55, v59, v36
	v_min_u32_e32 v58, v64, v58
	v_max_u32_e32 v64, v65, v56
	v_min_u32_e32 v56, v65, v56
	v_max_u32_e32 v65, v62, v60
	v_min_u32_e32 v60, v62, v60
	v_min_u32_e32 v36, v59, v36
	v_max_u32_e32 v59, v61, v43
	v_min_u32_e32 v43, v61, v43
	v_max_u32_e32 v61, v55, v37
	v_min_u32_e32 v37, v55, v37
	v_max_u32_e32 v62, v58, v42
	v_min_u32_e32 v42, v58, v42
	v_min_u32_e32 v58, v66, v63
	v_max_u32_e32 v67, v44, v60
	v_max_u32_e32 v55, v36, v35
	v_min_u32_e32 v35, v36, v35
	v_min_u32_e32 v36, v160, v57
	v_max_u32_e32 v161, v45, v37
	v_min_u32_e32 v44, v44, v60
	v_max_u32_e32 v60, v67, v58
	v_min_u32_e32 v58, v67, v58
	v_max_u32_e32 v67, v48, v56
	v_min_u32_e32 v48, v48, v56
	v_max_u32_e32 v56, v40, v42
	v_min_u32_e32 v37, v45, v37
	v_max_u32_e32 v45, v161, v36
	v_min_u32_e32 v36, v161, v36
	v_max_u32_e32 v161, v49, v43
	v_min_u32_e32 v43, v49, v43
	v_max_u32_e32 v49, v41, v35
	v_min_u32_e32 v40, v40, v42
	v_max_u32_e32 v42, v56, v48
	v_min_u32_e32 v48, v56, v48
	v_min_u32_e32 v35, v41, v35
	v_max_u32_e32 v41, v49, v43
	v_min_u32_e32 v43, v49, v43
	v_max_u32_e32 v56, v67, v60
	v_min_u32_e32 v60, v67, v60
	v_max_u32_e32 v67, v42, v58
	v_min_u32_e32 v42, v42, v58
	v_max_u32_e32 v58, v48, v44
	v_min_u32_e32 v44, v48, v44
	v_max_u32_e32 v48, v50, v64
	v_min_u32_e32 v50, v50, v64
	v_max_u32_e32 v64, v46, v62
	v_max_u32_e32 v49, v161, v45
	v_min_u32_e32 v45, v161, v45
	v_max_u32_e32 v161, v41, v36
	v_min_u32_e32 v36, v41, v36
	v_max_u32_e32 v41, v43, v37
	v_min_u32_e32 v37, v43, v37
	v_max_u32_e32 v43, v51, v59
	v_min_u32_e32 v51, v51, v59
	v_max_u32_e32 v59, v47, v55
	v_min_u32_e32 v46, v46, v62
	v_max_u32_e32 v62, v64, v50
	v_min_u32_e32 v50, v64, v50
	v_max_u32_e32 v64, v52, v65
	v_min_u32_e32 v52, v52, v65
	v_max_u32_e32 v65, v38, v54
	v_min_u32_e32 v47, v47, v55
	v_max_u32_e32 v55, v59, v51
	v_min_u32_e32 v51, v59, v51
	v_max_u32_e32 v59, v53, v61
	v_min_u32_e32 v53, v53, v61
	v_max_u32_e32 v61, v39, v34
	v_min_u32_e32 v38, v38, v54
	v_max_u32_e32 v54, v65, v52
	v_min_u32_e32 v52, v65, v52
	v_min_u32_e32 v34, v39, v34
	v_max_u32_e32 v39, v61, v53
	v_min_u32_e32 v53, v61, v53
	v_max_u32_e32 v65, v64, v62
	v_min_u32_e32 v62, v64, v62
	v_max_u32_e32 v64, v54, v50
	v_min_u32_e32 v50, v54, v50
	v_max_u32_e32 v54, v52, v46
	v_min_u32_e32 v46, v52, v46
	v_max_u32_e32 v61, v59, v55
	v_min_u32_e32 v55, v59, v55
	v_max_u32_e32 v59, v39, v51
	v_min_u32_e32 v39, v39, v51
	v_max_u32_e32 v51, v53, v47
	v_min_u32_e32 v47, v53, v47
	v_min_u32_e32 v52, v48, v56
	v_min_u32_e32 v68, v65, v60
	v_min_u32_e32 v69, v62, v67
	v_min_u32_e32 v96, v64, v42
	v_min_u32_e32 v97, v50, v58
	v_min_u32_e32 v158, v54, v44
	v_min_u32_e32 v159, v46, v40
	v_min_u32_e32 v53, v43, v49
	v_min_u32_e32 v162, v61, v45
	v_min_u32_e32 v163, v55, v161
	v_min_u32_e32 v164, v59, v36
	v_min_u32_e32 v165, v39, v41
	v_min_u32_e32 v166, v51, v37
	v_min_u32_e32 v167, v47, v35
	v_max3_u32 v34, v66, v63, v34
	v_max3_u32 v48, v48, v56, v167
	v_max3_u32 v35, v52, v47, v35
	v_max3_u32 v47, v65, v60, v166
	v_max3_u32 v37, v68, v51, v37
	v_max3_u32 v51, v62, v67, v165
	v_max3_u32 v39, v69, v39, v41
	v_max3_u32 v41, v64, v42, v164
	v_max3_u32 v36, v96, v59, v36
	v_max3_u32 v42, v50, v58, v163
	v_max3_u32 v50, v97, v55, v161
	v_max3_u32 v44, v54, v44, v162
	v_max3_u32 v45, v158, v61, v45
	v_max3_u32 v40, v46, v40, v53
	v_max3_u32 v43, v159, v43, v49
	v_max3_u32 v38, v38, v160, v57
	v_max_u32_e32 v46, v34, v36
	v_min_u32_e32 v34, v34, v36
	v_max_u32_e32 v36, v48, v42
	v_min_u32_e32 v42, v48, v42
; __device__ __forceinline__ void topk_phase(LAS unsigned char* lds, const bf16_t* qp, const bf16_t* keys, const float* SU, const float* SV, int* sel_e, float* sel_g, float* sel_su, int G, int b) {
;     ...
;             for (int i = 0; i < 16; ++i) T[p][i] = umax_(T[p][i], lo16[15 - i]);
;             SN_BITONIC16(T[p]);
;             TOPK_XMERGE(T[p], 16); TOPK_XMERGE(T[p], 32);
	v_max_u32_e32 v48, v35, v50
	v_min_u32_e32 v35, v35, v50
	v_max_u32_e32 v49, v47, v44
	v_min_u32_e32 v44, v47, v44
	v_max_u32_e32 v47, v37, v45
	v_min_u32_e32 v37, v37, v45
	v_max_u32_e32 v45, v51, v40
	v_min_u32_e32 v40, v51, v40
	v_max_u32_e32 v50, v39, v43
	v_min_u32_e32 v39, v39, v43
	v_max_u32_e32 v43, v41, v38
	v_min_u32_e32 v38, v41, v38
	v_max_u32_e32 v41, v46, v47
	v_min_u32_e32 v46, v46, v47
	v_max_u32_e32 v47, v36, v45
	v_min_u32_e32 v36, v36, v45
	v_max_u32_e32 v45, v48, v50
	v_min_u32_e32 v48, v48, v50
	v_max_u32_e32 v50, v49, v43
	v_min_u32_e32 v43, v49, v43
	v_max_u32_e32 v49, v34, v37
	v_min_u32_e32 v34, v34, v37
	v_max_u32_e32 v37, v42, v40
	v_min_u32_e32 v40, v42, v40
	v_max_u32_e32 v42, v35, v39
	v_min_u32_e32 v35, v35, v39
	v_max_u32_e32 v39, v44, v38
	v_min_u32_e32 v38, v44, v38
	v_max_u32_e32 v44, v41, v45
	v_min_u32_e32 v41, v41, v45
	v_max_u32_e32 v45, v47, v50
	v_min_u32_e32 v47, v47, v50
	v_max_u32_e32 v50, v46, v48
	v_min_u32_e32 v46, v46, v48
	v_max_u32_e32 v48, v36, v43
	v_min_u32_e32 v36, v36, v43
	v_max_u32_e32 v43, v49, v42
	v_min_u32_e32 v42, v49, v42
	v_max_u32_e32 v49, v37, v39
	v_min_u32_e32 v37, v37, v39
	v_max_u32_e32 v39, v34, v35
	v_min_u32_e32 v34, v34, v35
	v_max_u32_e32 v35, v40, v38
	v_min_u32_e32 v38, v40, v38
	v_max_u32_e32 v40, v44, v45
	v_min_u32_e32 v44, v44, v45
	v_max_u32_e32 v45, v41, v47
	v_min_u32_e32 v41, v41, v47
	v_max_u32_e32 v47, v50, v48
	v_min_u32_e32 v48, v50, v48
	v_max_u32_e32 v50, v46, v36
	v_min_u32_e32 v36, v46, v36
	v_max_u32_e32 v46, v43, v49
	v_min_u32_e32 v43, v43, v49
	v_max_u32_e32 v49, v42, v37
	v_min_u32_e32 v37, v42, v37
	v_max_u32_e32 v42, v39, v35
	v_min_u32_e32 v35, v39, v35
	v_max_u32_e32 v39, v34, v38
	v_min_u32_e32 v34, v34, v38
	v_mov_b32_e32 v38, v40
	v_mov_b32_e32 v51, v44
	v_mov_b32_e32 v52, v45
	v_mov_b32_e32 v53, v41
	v_mov_b32_e32 v54, v47
	v_mov_b32_e32 v55, v48
	v_mov_b32_e32 v56, v50
	v_mov_b32_e32 v57, v36
	v_mov_b32_e32 v58, v46
	v_mov_b32_e32 v59, v43
	v_mov_b32_e32 v60, v49
	v_mov_b32_e32 v61, v37
	v_mov_b32_e32 v62, v42
	v_mov_b32_e32 v63, v35
	v_mov_b32_e32 v64, v39
	v_mov_b32_e32 v65, v34
	v_permlane16_swap_b32_e32 v40, v38
	v_permlane16_swap_b32_e32 v44, v51
	v_permlane16_swap_b32_e32 v45, v52
	v_permlane16_swap_b32_e32 v41, v53
	v_permlane16_swap_b32_e32 v47, v54
	v_permlane16_swap_b32_e32 v48, v55
	v_permlane16_swap_b32_e32 v50, v56
	v_permlane16_swap_b32_e32 v36, v57
	v_permlane16_swap_b32_e32 v46, v58
	v_permlane16_swap_b32_e32 v43, v59
	v_permlane16_swap_b32_e32 v49, v60
	v_permlane16_swap_b32_e32 v37, v61
	v_permlane16_swap_b32_e32 v42, v62
	v_permlane16_swap_b32_e32 v35, v63
	v_permlane16_swap_b32_e32 v39, v64
	v_permlane16_swap_b32_e32 v34, v65
	v_max_u32_e32 v40, v40, v65
	v_max_u32_e32 v44, v44, v64
	v_max_u32_e32 v45, v45, v63
	v_max_u32_e32 v41, v41, v62
	v_max_u32_e32 v47, v47, v61
	v_max_u32_e32 v48, v48, v60
	v_max_u32_e32 v50, v50, v59
	v_max_u32_e32 v36, v36, v58
	v_max_u32_e32 v46, v46, v57
	v_max_u32_e32 v43, v43, v56
	v_max_u32_e32 v49, v49, v55
	v_max_u32_e32 v37, v37, v54
	v_max_u32_e32 v42, v42, v53
	v_max_u32_e32 v35, v35, v52
	v_max_u32_e32 v39, v39, v51
	v_max_u32_e32 v34, v34, v38
	v_max_u32_e32 v38, v40, v46
	v_min_u32_e32 v40, v40, v46
	v_max_u32_e32 v46, v44, v43
	v_min_u32_e32 v43, v44, v43
	v_max_u32_e32 v44, v45, v49
	v_min_u32_e32 v45, v45, v49
	v_max_u32_e32 v49, v41, v37
	v_min_u32_e32 v37, v41, v37
	v_max_u32_e32 v41, v47, v42
	v_min_u32_e32 v42, v47, v42
	v_max_u32_e32 v47, v48, v35
	v_min_u32_e32 v35, v48, v35
	v_max_u32_e32 v48, v50, v39
	v_min_u32_e32 v39, v50, v39
	v_max_u32_e32 v50, v36, v34
	v_min_u32_e32 v34, v36, v34
	v_max_u32_e32 v36, v38, v41
	v_min_u32_e32 v38, v38, v41
	v_max_u32_e32 v41, v46, v47
	v_min_u32_e32 v46, v46, v47
	v_max_u32_e32 v47, v44, v48
	v_min_u32_e32 v44, v44, v48
	v_max_u32_e32 v48, v49, v50
	v_min_u32_e32 v49, v49, v50
	v_max_u32_e32 v50, v40, v42
	v_min_u32_e32 v40, v40, v42
	v_max_u32_e32 v42, v43, v35
	v_min_u32_e32 v35, v43, v35
	v_max_u32_e32 v43, v45, v39
	v_min_u32_e32 v39, v45, v39
	v_max_u32_e32 v45, v37, v34
	v_min_u32_e32 v34, v37, v34
	v_max_u32_e32 v37, v36, v47
	v_min_u32_e32 v47, v36, v47
	v_max_u32_e32 v51, v41, v48
	v_min_u32_e32 v41, v41, v48
	v_max_u32_e32 v48, v38, v44
	v_min_u32_e32 v44, v38, v44
	v_max_u32_e32 v52, v46, v49
	v_min_u32_e32 v46, v46, v49
	v_max_u32_e32 v49, v50, v43
	v_min_u32_e32 v50, v50, v43
	v_max_u32_e32 v53, v42, v45
	v_min_u32_e32 v55, v42, v45
	v_max_u32_e32 v58, v40, v39
	v_min_u32_e32 v59, v40, v39
	v_max_u32_e32 v60, v35, v34
	v_min_u32_e32 v34, v35, v34
	v_max_u32_e32 v36, v37, v51
	v_min_u32_e32 v37, v37, v51
	v_max_u32_e32 v38, v47, v41
	v_min_u32_e32 v39, v47, v41
	v_max_u32_e32 v40, v48, v52
	v_min_u32_e32 v41, v48, v52
	v_max_u32_e32 v42, v44, v46
	v_min_u32_e32 v43, v44, v46
	v_max_u32_e32 v44, v49, v53
	v_min_u32_e32 v45, v49, v53
	v_max_u32_e32 v54, v50, v55
	v_min_u32_e32 v56, v50, v55
	v_max_u32_e32 v57, v58, v60
	v_min_u32_e32 v66, v58, v60
	v_max_u32_e32 v67, v59, v34
	v_min_u32_e32 v68, v59, v34
	v_mov_b32_e32 v69, v36
	v_mov_b32_e32 v158, v37
	v_mov_b32_e32 v159, v38
	v_mov_b32_e32 v160, v39
	v_mov_b32_e32 v161, v40
	v_mov_b32_e32 v162, v41
	v_mov_b32_e32 v163, v42
	v_mov_b32_e32 v97, v43
	v_mov_b32_e32 v53, v44
	v_mov_b32_e32 v52, v45
	v_mov_b32_e32 v51, v54
	v_mov_b32_e32 v50, v56
	v_mov_b32_e32 v49, v57
	v_mov_b32_e32 v48, v66
	v_mov_b32_e32 v47, v67
	v_mov_b32_e32 v46, v68
	v_permlane32_swap_b32_e32 v36, v69
	v_permlane32_swap_b32_e32 v37, v158
	v_permlane32_swap_b32_e32 v38, v159
	v_permlane32_swap_b32_e32 v39, v160
	v_permlane32_swap_b32_e32 v40, v161
	v_permlane32_swap_b32_e32 v41, v162
; __device__ __forceinline__ void topk_phase(LAS unsigned char* lds, const bf16_t* qp, const bf16_t* keys, const float* SU, const float* SV, int* sel_e, float* sel_g, float* sel_su, int G, int b) {
;     ...
;             TOPK_XMERGE(T[p], 16); TOPK_XMERGE(T[p], 32);
	v_permlane32_swap_b32_e32 v42, v163
	v_permlane32_swap_b32_e32 v43, v97
	v_permlane32_swap_b32_e32 v44, v53
	v_permlane32_swap_b32_e32 v45, v52
	v_permlane32_swap_b32_e32 v54, v51
	v_permlane32_swap_b32_e32 v56, v50
	v_permlane32_swap_b32_e32 v57, v49
	v_permlane32_swap_b32_e32 v66, v48
	v_permlane32_swap_b32_e32 v67, v47
	v_permlane32_swap_b32_e32 v68, v46
	v_max_u32_e32 v59, v70, v157
	v_max_u32_e32 v60, v71, v156
	v_max_u32_e32 v61, v72, v155
	v_max_u32_e32 v62, v73, v154
	v_max_u32_e32 v63, v74, v153
	v_max_u32_e32 v64, v75, v152
	v_max_u32_e32 v65, v76, v151
	v_max_u32_e32 v70, v77, v150
	v_max_u32_e32 v71, v134, v149
	v_max_u32_e32 v72, v135, v148
	v_max_u32_e32 v73, v136, v147
	v_max_u32_e32 v74, v137, v146
	v_max_u32_e32 v75, v138, v145
	v_max_u32_e32 v76, v139, v144
	v_max_u32_e32 v77, v140, v143
	v_max_u32_e32 v96, v141, v142
	v_max_u32_e32 v46, v36, v46
	v_max_u32_e32 v47, v37, v47
	v_max_u32_e32 v48, v38, v48
	v_max_u32_e32 v49, v39, v49
	v_max_u32_e32 v50, v40, v50
	v_max_u32_e32 v51, v41, v51
	v_max_u32_e32 v52, v42, v52
	v_max_u32_e32 v53, v43, v53
	v_max_u32_e32 v97, v44, v97
	v_max_u32_e32 v134, v45, v163
	v_max_u32_e32 v143, v54, v162
	v_max_u32_e32 v149, v56, v161
	v_max_u32_e32 v150, v57, v160
	v_max_u32_e32 v151, v66, v159
	v_max_u32_e32 v152, v67, v158
	v_max_u32_e32 v153, v68, v69
	v_max_u32_e32 v216, v59, v71
	v_min_u32_e32 v224, v59, v71
	v_max_u32_e32 v217, v60, v72
	v_min_u32_e32 v225, v60, v72
	v_max_u32_e32 v218, v61, v73
	v_min_u32_e32 v226, v61, v73
	v_max_u32_e32 v219, v62, v74
	v_min_u32_e32 v227, v62, v74
	v_max_u32_e32 v220, v63, v75
	v_min_u32_e32 v228, v63, v75
	v_max_u32_e32 v221, v64, v76
	v_min_u32_e32 v229, v64, v76
	v_max_u32_e32 v222, v65, v77
	v_min_u32_e32 v230, v65, v77
	v_max_u32_e32 v223, v70, v96
	v_min_u32_e32 v231, v70, v96
	v_max_u32_e32 v232, v216, v220
	v_min_u32_e32 v236, v216, v220
	v_max_u32_e32 v233, v217, v221
	v_min_u32_e32 v237, v217, v221
	v_max_u32_e32 v234, v218, v222
	v_min_u32_e32 v238, v218, v222
	v_max_u32_e32 v235, v219, v223
	v_min_u32_e32 v239, v219, v223
	v_max_u32_e32 v240, v224, v228
	v_min_u32_e32 v246, v224, v228
	v_max_u32_e32 v241, v225, v229
	v_min_u32_e32 v247, v225, v229
	v_max_u32_e32 v244, v226, v230
	v_min_u32_e32 v248, v226, v230
	v_max_u32_e32 v245, v227, v231
	v_min_u32_e32 v249, v227, v231
	v_max_u32_e32 v216, v232, v234
	v_min_u32_e32 v218, v232, v234
	v_max_u32_e32 v217, v233, v235
	v_min_u32_e32 v219, v233, v235
	v_max_u32_e32 v220, v236, v238
	v_min_u32_e32 v222, v236, v238
	v_max_u32_e32 v221, v237, v239
	v_min_u32_e32 v223, v237, v239
	v_max_u32_e32 v224, v240, v244
	v_min_u32_e32 v226, v240, v244
	v_max_u32_e32 v225, v241, v245
	v_min_u32_e32 v227, v241, v245
	v_max_u32_e32 v228, v246, v248
	v_min_u32_e32 v230, v246, v248
	v_max_u32_e32 v229, v247, v249
	v_min_u32_e32 v231, v247, v249
	v_max_u32_e32 v34, v216, v217
	v_min_u32_e32 v35, v216, v217
	v_max_u32_e32 v36, v218, v219
	v_min_u32_e32 v37, v218, v219
	v_max_u32_e32 v54, v220, v221
	v_min_u32_e32 v55, v220, v221
	v_max_u32_e32 v56, v222, v223
	v_min_u32_e32 v57, v222, v223
	v_max_u32_e32 v58, v224, v225
	v_min_u32_e32 v59, v224, v225
	v_max_u32_e32 v60, v226, v227
	v_min_u32_e32 v61, v226, v227
	v_max_u32_e32 v62, v228, v229
	v_min_u32_e32 v63, v228, v229
	v_max_u32_e32 v64, v230, v231
	v_min_u32_e32 v65, v230, v231
	v_max_u32_e32 v216, v46, v97
	v_min_u32_e32 v224, v46, v97
	v_max_u32_e32 v217, v47, v134
	v_min_u32_e32 v225, v47, v134
	v_max_u32_e32 v218, v48, v143
	v_min_u32_e32 v226, v48, v143
	v_max_u32_e32 v219, v49, v149
	v_min_u32_e32 v227, v49, v149
	v_max_u32_e32 v220, v50, v150
	v_min_u32_e32 v228, v50, v150
	v_max_u32_e32 v221, v51, v151
	v_min_u32_e32 v229, v51, v151
	v_max_u32_e32 v222, v52, v152
	v_min_u32_e32 v230, v52, v152
	v_max_u32_e32 v223, v53, v153
	v_min_u32_e32 v231, v53, v153
	v_max_u32_e32 v232, v216, v220
	v_min_u32_e32 v236, v216, v220
	v_max_u32_e32 v233, v217, v221
	v_min_u32_e32 v237, v217, v221
	v_max_u32_e32 v234, v218, v222
	v_min_u32_e32 v238, v218, v222
	v_max_u32_e32 v235, v219, v223
	v_min_u32_e32 v239, v219, v223
	v_max_u32_e32 v240, v224, v228
	v_min_u32_e32 v246, v224, v228
	v_max_u32_e32 v241, v225, v229
	v_min_u32_e32 v247, v225, v229
	v_max_u32_e32 v244, v226, v230
	v_min_u32_e32 v248, v226, v230
	v_max_u32_e32 v245, v227, v231
	v_min_u32_e32 v249, v227, v231
	v_max_u32_e32 v216, v232, v234
	v_min_u32_e32 v218, v232, v234
	v_max_u32_e32 v217, v233, v235
	v_min_u32_e32 v219, v233, v235
	v_max_u32_e32 v220, v236, v238
	v_min_u32_e32 v222, v236, v238
	v_max_u32_e32 v221, v237, v239
	v_min_u32_e32 v223, v237, v239
	v_max_u32_e32 v224, v240, v244
	v_min_u32_e32 v226, v240, v244
	v_max_u32_e32 v225, v241, v245
	v_min_u32_e32 v227, v241, v245
	v_max_u32_e32 v228, v246, v248
	v_min_u32_e32 v230, v246, v248
	v_max_u32_e32 v229, v247, v249
	v_min_u32_e32 v231, v247, v249
	v_max_u32_e32 v38, v216, v217
	v_min_u32_e32 v39, v216, v217
	v_max_u32_e32 v40, v218, v219
	v_min_u32_e32 v41, v218, v219
	v_max_u32_e32 v42, v220, v221
	v_min_u32_e32 v43, v220, v221
	v_max_u32_e32 v44, v222, v223
	v_min_u32_e32 v45, v222, v223
	v_max_u32_e32 v46, v224, v225
	v_min_u32_e32 v47, v224, v225
	v_max_u32_e32 v48, v226, v227
	v_min_u32_e32 v49, v226, v227
	v_max_u32_e32 v50, v228, v229
	v_min_u32_e32 v51, v228, v229
	v_max_u32_e32 v52, v230, v231
	v_min_u32_e32 v53, v230, v231
	v_ashrrev_i32_e32 v216, 31, v34
	v_ashrrev_i32_e32 v217, 31, v35
	v_ashrrev_i32_e32 v218, 31, v36
	v_ashrrev_i32_e32 v219, 31, v37
	v_ashrrev_i32_e32 v220, 31, v54
	v_ashrrev_i32_e32 v221, 31, v55
	v_ashrrev_i32_e32 v222, 31, v56
	v_ashrrev_i32_e32 v223, 31, v57
	v_ashrrev_i32_e32 v224, 31, v58
; __device__ __forceinline__ unsigned mono(float f) { const unsigned u = __float_as_uint(f); return (u & 0x80000000u) ? ~u : (u ^ 0x80000000u); }
; __device__ __forceinline__ float unmono(unsigned u) { return __uint_as_float((u & 0x80000000u) ? (u ^ 0x80000000u) : ~u); }
; __device__ __forceinline__ void topk_phase(LAS unsigned char* lds, const bf16_t* qp, const bf16_t* keys, const float* SU, const float* SV, int* sel_e, float* sel_g, float* sel_su, int G, int b) {
;     ...
;         float v1[16], v2[16];
; #pragma unroll
;         for (int i = 0; i < 16; ++i) { v1[i] = unmono(T[0][i] & ~127u); v2[i] = unmono(T[1][i] & ~127u); }
;         unsigned ck[16];
; #pragma unroll
;         for (int sidx = 0; sidx < 13; ++sidx) {
;             unsigned keyk[4];
; #pragma unroll
;             for (int k = 0; k < 4; ++k) {
;                 const int c = 4 * sidx + k;
;                 if (c < 50) { const int ci = cand_i(c), cj = cand_j(c); keyk[k] = (mono(v1[ci] + v2[cj]) & ~255u) | (unsigned)(255 - (ci * 16 + cj)); }
;                 else keyk[k] = 0u;
;             }
;             ck[sidx] = fq == 0 ? keyk[0] : fq == 1 ? keyk[1] : fq == 2 ? keyk[2] : keyk[3];
;         }
	v_ashrrev_i32_e32 v225, 31, v59
	v_ashrrev_i32_e32 v226, 31, v60
	v_ashrrev_i32_e32 v227, 31, v61
	v_ashrrev_i32_e32 v228, 31, v62
	v_ashrrev_i32_e32 v229, 31, v63
	v_ashrrev_i32_e32 v230, 31, v64
	v_ashrrev_i32_e32 v231, 31, v65
	v_bitop3_b32 v170, v34, v216, s12 bitop3:0x93
	v_bitop3_b32 v171, v35, v217, s12 bitop3:0x93
	v_bitop3_b32 v172, v36, v218, s12 bitop3:0x93
	v_bitop3_b32 v173, v37, v219, s12 bitop3:0x93
	v_bitop3_b32 v174, v54, v220, s12 bitop3:0x93
	v_bitop3_b32 v175, v55, v221, s12 bitop3:0x93
	v_bitop3_b32 v176, v56, v222, s12 bitop3:0x93
	v_bitop3_b32 v177, v57, v223, s12 bitop3:0x93
	v_bitop3_b32 v178, v58, v224, s12 bitop3:0x93
	v_bitop3_b32 v179, v59, v225, s12 bitop3:0x93
	v_bitop3_b32 v180, v60, v226, s12 bitop3:0x93
	v_bitop3_b32 v181, v61, v227, s12 bitop3:0x93
	v_bitop3_b32 v182, v62, v228, s12 bitop3:0x93
	v_bitop3_b32 v183, v63, v229, s12 bitop3:0x93
	v_bitop3_b32 v184, v64, v230, s12 bitop3:0x93
	v_bitop3_b32 v185, v65, v231, s12 bitop3:0x93
	v_ashrrev_i32_e32 v216, 31, v38
	v_ashrrev_i32_e32 v217, 31, v39
	v_ashrrev_i32_e32 v218, 31, v40
	v_ashrrev_i32_e32 v219, 31, v41
	v_ashrrev_i32_e32 v220, 31, v42
	v_ashrrev_i32_e32 v221, 31, v43
	v_ashrrev_i32_e32 v222, 31, v44
	v_ashrrev_i32_e32 v223, 31, v45
	v_ashrrev_i32_e32 v224, 31, v46
	v_ashrrev_i32_e32 v225, 31, v47
	v_ashrrev_i32_e32 v226, 31, v48
	v_ashrrev_i32_e32 v227, 31, v49
	v_ashrrev_i32_e32 v228, 31, v50
	v_ashrrev_i32_e32 v229, 31, v51
	v_ashrrev_i32_e32 v230, 31, v52
	v_ashrrev_i32_e32 v231, 31, v53
	v_bitop3_b32 v186, v38, v216, s12 bitop3:0x93
	v_bitop3_b32 v187, v39, v217, s12 bitop3:0x93
	v_bitop3_b32 v188, v40, v218, s12 bitop3:0x93
	v_bitop3_b32 v189, v41, v219, s12 bitop3:0x93
	v_bitop3_b32 v190, v42, v220, s12 bitop3:0x93
	v_bitop3_b32 v191, v43, v221, s12 bitop3:0x93
	v_bitop3_b32 v192, v44, v222, s12 bitop3:0x93
	v_bitop3_b32 v193, v45, v223, s12 bitop3:0x93
	v_bitop3_b32 v194, v46, v224, s12 bitop3:0x93
	v_bitop3_b32 v195, v47, v225, s12 bitop3:0x93
	v_bitop3_b32 v196, v48, v226, s12 bitop3:0x93
	v_bitop3_b32 v197, v49, v227, s12 bitop3:0x93
	v_bitop3_b32 v198, v50, v228, s12 bitop3:0x93
	v_bitop3_b32 v199, v51, v229, s12 bitop3:0x93
	v_bitop3_b32 v200, v52, v230, s12 bitop3:0x93
	v_bitop3_b32 v201, v53, v231, s12 bitop3:0x93
	v_cndmask_b32_e64 v250, v186, v187, s[16:17]
	v_cndmask_b32_e64 v250, v250, v188, s[18:19]
	v_cndmask_b32_e64 v250, v250, v189, s[20:21]
	v_cndmask_b32_e64 v251, v190, v191, s[16:17]
	v_cndmask_b32_e64 v251, v251, v192, s[18:19]
	v_cndmask_b32_e64 v251, v251, v193, s[20:21]
	v_cndmask_b32_e64 v252, v194, v195, s[16:17]
	v_cndmask_b32_e64 v252, v252, v196, s[18:19]
	v_cndmask_b32_e64 v252, v252, v197, s[20:21]
	v_cndmask_b32_e64 v253, v198, v199, s[16:17]
	v_cndmask_b32_e64 v253, v253, v200, s[18:19]
	v_cndmask_b32_e64 v253, v253, v201, s[20:21]
	v_add_f32_e32 v254, v170, v250
	v_ashrrev_i32_e32 v255, 31, v254
	v_bitop3_b32 v254, v254, v255, v132 bitop3:0x1e
	v_and_or_b32 v68, v254, s60, v203
	v_add_f32_e32 v254, v170, v251
	v_ashrrev_i32_e32 v255, 31, v254
	v_bitop3_b32 v254, v254, v255, v132 bitop3:0x1e
	v_and_or_b32 v69, v254, s60, v204
	v_add_f32_e32 v254, v170, v252
	v_ashrrev_i32_e32 v255, 31, v254
	v_bitop3_b32 v254, v254, v255, v132 bitop3:0x1e
	v_and_or_b32 v97, v254, s60, v205
	v_add_f32_e32 v254, v170, v253
	v_ashrrev_i32_e32 v255, 31, v254
	v_bitop3_b32 v254, v254, v255, v132 bitop3:0x1e
	v_and_or_b32 v134, v254, s60, v206
	v_add_f32_e32 v254, v171, v250
	v_ashrrev_i32_e32 v255, 31, v254
	v_bitop3_b32 v254, v254, v255, v132 bitop3:0x1e
	v_and_or_b32 v142, v254, s60, v207
	v_add_f32_e32 v254, v171, v251
	v_ashrrev_i32_e32 v255, 31, v254
	v_bitop3_b32 v254, v254, v255, v132 bitop3:0x1e
	v_and_or_b32 v143, v254, s60, v208
	v_add_f32_e32 v254, v172, v250
	v_ashrrev_i32_e32 v255, 31, v254
	v_bitop3_b32 v254, v254, v255, v132 bitop3:0x1e
	v_and_or_b32 v144, v254, s60, v209
	v_cndmask_b32_e64 v232, v172, v173, s[16:17]
	v_cndmask_b32_e64 v232, v232, v173, s[22:23]
	v_cndmask_b32_e64 v233, v190, v186, s[16:17]
	v_cndmask_b32_e64 v233, v233, v187, s[18:19]
	v_cndmask_b32_e64 v233, v233, v188, s[20:21]
	v_add_f32_e32 v254, v232, v233
	v_ashrrev_i32_e32 v255, 31, v254
	v_bitop3_b32 v254, v254, v255, v132 bitop3:0x1e
	v_and_or_b32 v145, v254, s60, v210
	v_cndmask_b32_e64 v234, v173, v174, s[16:17]
	v_cndmask_b32_e64 v234, v234, v174, s[22:23]
	v_cndmask_b32_e64 v235, v189, v186, s[16:17]
	v_cndmask_b32_e64 v235, v235, v187, s[18:19]
	v_cndmask_b32_e64 v235, v235, v188, s[20:21]
	v_add_f32_e32 v254, v234, v235
	v_ashrrev_i32_e32 v255, 31, v254
	v_bitop3_b32 v254, v254, v255, v132 bitop3:0x1e
	v_and_or_b32 v135, v254, s60, v211
	v_cndmask_b32_e64 v236, v175, v176, s[22:23]
	v_cndmask_b32_e64 v237, v186, v187, s[24:25]
	v_add_f32_e32 v254, v236, v237
	v_ashrrev_i32_e32 v255, 31, v254
	v_bitop3_b32 v254, v254, v255, v132 bitop3:0x1e
	v_and_or_b32 v136, v254, s60, v212
	v_cndmask_b32_e64 v238, v177, v178, s[18:19]
	v_cndmask_b32_e64 v238, v238, v179, s[20:21]
	v_cndmask_b32_e64 v239, v186, v187, s[16:17]
	v_add_f32_e32 v254, v238, v239
	v_ashrrev_i32_e32 v255, 31, v254
	v_bitop3_b32 v254, v254, v255, v132 bitop3:0x1e
	v_and_or_b32 v70, v254, s60, v213
	v_cndmask_b32_e64 v240, v180, v181, s[16:17]
	v_cndmask_b32_e64 v240, v240, v182, s[18:19]
	v_cndmask_b32_e64 v240, v240, v183, s[20:21]
	v_add_f32_e32 v254, v240, v186
	v_ashrrev_i32_e32 v255, 31, v254
	v_bitop3_b32 v254, v254, v255, v132 bitop3:0x1e
	v_and_or_b32 v71, v254, s60, v214
	v_cndmask_b32_e64 v241, v184, v185, s[16:17]
	v_add_f32_e32 v254, v241, v186
	v_ashrrev_i32_e32 v255, 31, v254
	v_bitop3_b32 v254, v254, v255, v132 bitop3:0x1e
	v_and_or_b32 v67, v254, s60, v215
; __device__ __forceinline__ unsigned mono(float f) { const unsigned u = __float_as_uint(f); return (u & 0x80000000u) ? ~u : (u ^ 0x80000000u); }
; __device__ __forceinline__ void topk_phase(LAS unsigned char* lds, const bf16_t* qp, const bf16_t* keys, const float* SU, const float* SV, int* sel_e, float* sel_g, float* sel_su, int G, int b) {
;     ...
;                 const int c = 4 * sidx + k;
;                 if (c < 50) { const int ci = cand_i(c), cj = cand_j(c); keyk[k] = (mono(v1[ci] + v2[cj]) & ~255u) | (unsigned)(255 - (ci * 16 + cj)); }
;                 else keyk[k] = 0u;
;             }
;             ck[sidx] = fq == 0 ? keyk[0] : fq == 1 ? keyk[1] : fq == 2 ? keyk[2] : keyk[3];
;         }
;         ck[13] = 0u; ck[14] = 0u; ck[15] = 0u;
;         SN_SORT16(ck);
;         TOPK_XMERGE(ck, 16); TOPK_XMERGE(ck, 32);
	v_cndmask_b32_e64 v67, v67, 0, s[22:23]
	v_max_u32_e32 v66, v68, v69
	v_min_u32_e32 v68, v68, v69
	v_max_u32_e32 v69, v97, v134
	v_min_u32_e32 v72, v97, v134
	v_max_u32_e32 v73, v66, v69
	v_min_u32_e32 v66, v66, v69
	v_max_u32_e32 v69, v68, v72
	v_min_u32_e32 v68, v68, v72
	v_max_u32_e32 v72, v69, v66
	v_min_u32_e32 v66, v69, v66
	v_max_u32_e32 v69, v142, v143
	v_min_u32_e32 v74, v142, v143
	v_max_u32_e32 v75, v144, v145
	v_min_u32_e32 v76, v144, v145
	v_max_u32_e32 v77, v69, v75
	v_min_u32_e32 v69, v69, v75
	v_max_u32_e32 v75, v74, v76
	v_min_u32_e32 v74, v74, v76
	v_max_u32_e32 v76, v75, v69
	v_min_u32_e32 v69, v75, v69
	v_max_u32_e32 v75, v73, v77
	v_min_u32_e32 v73, v73, v77
	v_max_u32_e32 v77, v66, v69
	v_min_u32_e32 v66, v66, v69
	v_max_u32_e32 v69, v77, v73
	v_min_u32_e32 v73, v77, v73
	v_max_u32_e32 v77, v72, v76
	v_min_u32_e32 v72, v72, v76
	v_max_u32_e32 v76, v68, v74
	v_min_u32_e32 v68, v68, v74
	v_max_u32_e32 v74, v76, v72
	v_min_u32_e32 v72, v76, v72
	v_max_u32_e32 v76, v77, v69
	v_min_u32_e32 v69, v77, v69
	v_max_u32_e32 v77, v74, v73
	v_min_u32_e32 v73, v74, v73
	v_max_u32_e32 v74, v72, v66
	v_min_u32_e32 v66, v72, v66
	v_max_u32_e32 v72, v135, v136
	v_min_u32_e32 v96, v135, v136
	v_max_u32_e32 v97, v70, v71
	v_min_u32_e32 v70, v70, v71
	v_max_u32_e32 v71, v72, v97
	v_min_u32_e32 v72, v72, v97
	v_max_u32_e32 v97, v96, v70
	v_min_u32_e32 v134, v97, v72
	v_max_u32_e32 v135, v71, v67
	v_min_u32_e32 v67, v71, v67
	v_min_u32_e32 v70, v96, v70
	v_max_u32_e32 v71, v134, v67
	v_min_u32_e32 v134, v134, v67
	v_max_u32_e32 v96, v97, v72
	v_med3_u32 v67, v97, v72, v67
	v_max_u32_e32 v72, v70, v134
	v_min_u32_e32 v70, v70, v134
	v_max_u32_e32 v71, v96, v71
	v_max_u32_e32 v96, v75, v135
	v_min_u32_e32 v75, v75, v135
	v_max_u32_e32 v97, v73, v70
	v_min_u32_e32 v70, v73, v70
	v_max_u32_e32 v73, v97, v75
	v_min_u32_e32 v75, v97, v75
	v_max_u32_e32 v97, v69, v67
	v_min_u32_e32 v67, v69, v67
	v_max_u32_e32 v69, v66, v67
	v_min_u32_e32 v66, v66, v67
	v_max_u32_e32 v67, v97, v73
	v_min_u32_e32 v73, v97, v73
	v_max_u32_e32 v97, v69, v75
	v_min_u32_e32 v69, v69, v75
	v_max_u32_e32 v75, v66, v70
	v_min_u32_e32 v66, v66, v70
	v_max_u32_e32 v70, v76, v71
	v_min_u32_e32 v71, v76, v71
	v_max_u32_e32 v76, v74, v71
	v_min_u32_e32 v71, v74, v71
	v_max_u32_e32 v74, v77, v72
	v_min_u32_e32 v72, v77, v72
	v_max_u32_e32 v77, v68, v72
	v_min_u32_e32 v68, v68, v72
	v_max_u32_e32 v72, v74, v76
	v_min_u32_e32 v74, v74, v76
	v_max_u32_e32 v76, v77, v71
	v_min_u32_e32 v71, v77, v71
	v_max_u32_e32 v77, v70, v67
	v_min_u32_e32 v67, v70, v67
	v_max_u32_e32 v70, v72, v73
	v_min_u32_e32 v72, v72, v73
	v_max_u32_e32 v73, v74, v97
	v_min_u32_e32 v74, v74, v97
	v_max_u32_e32 v97, v76, v69
	v_min_u32_e32 v69, v76, v69
	v_max_u32_e32 v76, v71, v75
	v_min_u32_e32 v71, v71, v75
	v_max_u32_e32 v75, v68, v66
	v_min_u32_e32 v66, v68, v66
	v_mov_b32_e32 v68, v96
	v_mov_b32_e32 v134, v77
	v_mov_b32_e32 v135, v67
	v_mov_b32_e32 v136, v70
	v_mov_b32_e32 v137, v72
	v_mov_b32_e32 v138, v73
	v_mov_b32_e32 v139, v74
	v_mov_b32_e32 v140, v97
	v_mov_b32_e32 v141, v69
	v_mov_b32_e32 v142, v76
	v_mov_b32_e32 v143, v71
	v_mov_b32_e32 v144, v75
	v_mov_b32_e32 v145, v66
	v_mov_b32_e32 v146, 0
	v_mov_b32_e32 v147, 0
	v_permlane16_swap_b32_e32 v96, v68
	v_permlane16_swap_b32_e32 v77, v134
	v_permlane16_swap_b32_e32 v67, v135
	v_permlane16_swap_b32_e32 v70, v136
	v_permlane16_swap_b32_e32 v72, v137
	v_permlane16_swap_b32_e32 v73, v138
	v_permlane16_swap_b32_e32 v74, v139
	v_permlane16_swap_b32_e32 v97, v140
	v_permlane16_swap_b32_e32 v69, v141
	v_permlane16_swap_b32_e32 v76, v142
	v_permlane16_swap_b32_e32 v71, v143
	v_permlane16_swap_b32_e32 v75, v144
	v_permlane16_swap_b32_e32 v66, v145
	v_permlane16_swap_b32_e32 v146, v147
; __device__ __forceinline__ void topk_phase(LAS unsigned char* lds, const bf16_t* qp, const bf16_t* keys, const float* SU, const float* SV, int* sel_e, float* sel_g, float* sel_su, int G, int b) {
;     ...
;         SN_SORT16(ck);
;         TOPK_XMERGE(ck, 16); TOPK_XMERGE(ck, 32);
;         if (fq == 0) {
; #pragma unroll
;             for (int i = 0; i < 16; ++i) { wl[i] = T[0][i]; wl[16 + i] = T[1][i]; }
;         }
	v_max_u32_e32 v96, v96, v147
	v_max_u32_e32 v77, v77, v147
	v_max_u32_e32 v67, v67, v147
	v_max_u32_e32 v70, v70, v145
	v_max_u32_e32 v72, v72, v144
	v_max_u32_e32 v73, v73, v143
	v_max_u32_e32 v74, v74, v142
	v_max_u32_e32 v97, v97, v141
	v_max_u32_e32 v69, v69, v140
	v_max_u32_e32 v76, v76, v139
	v_max_u32_e32 v71, v71, v138
	v_max_u32_e32 v75, v75, v137
	v_max_u32_e32 v66, v66, v136
	v_max_u32_e32 v135, v146, v135
	v_max_u32_e32 v134, v146, v134
	v_max_u32_e32 v68, v146, v68
	v_max_u32_e32 v136, v96, v69
	v_min_u32_e32 v69, v96, v69
	v_max_u32_e32 v96, v77, v76
	v_min_u32_e32 v76, v77, v76
	v_max_u32_e32 v77, v67, v71
	v_min_u32_e32 v67, v67, v71
	v_max_u32_e32 v71, v70, v75
	v_min_u32_e32 v70, v70, v75
	v_max_u32_e32 v75, v72, v66
	v_min_u32_e32 v66, v72, v66
	v_max_u32_e32 v72, v73, v135
	v_min_u32_e32 v73, v73, v135
	v_max_u32_e32 v135, v74, v134
	v_min_u32_e32 v74, v74, v134
	v_max_u32_e32 v134, v97, v68
	v_min_u32_e32 v68, v97, v68
	v_max_u32_e32 v97, v136, v75
	v_min_u32_e32 v75, v136, v75
	v_max_u32_e32 v136, v96, v72
	v_min_u32_e32 v72, v96, v72
	v_max_u32_e32 v96, v77, v135
	v_min_u32_e32 v77, v77, v135
	v_max_u32_e32 v135, v71, v134
	v_min_u32_e32 v71, v71, v134
	v_max_u32_e32 v134, v69, v66
	v_min_u32_e32 v66, v69, v66
	v_max_u32_e32 v69, v76, v73
	v_min_u32_e32 v73, v76, v73
	v_max_u32_e32 v76, v67, v74
	v_min_u32_e32 v67, v67, v74
	v_max_u32_e32 v74, v70, v68
	v_min_u32_e32 v68, v70, v68
	v_max_u32_e32 v70, v97, v96
	v_min_u32_e32 v96, v97, v96
	v_max_u32_e32 v97, v136, v135
	v_min_u32_e32 v135, v136, v135
	v_max_u32_e32 v136, v75, v77
	v_min_u32_e32 v75, v75, v77
	v_max_u32_e32 v77, v72, v71
	v_min_u32_e32 v137, v72, v71
	v_max_u32_e32 v138, v134, v76
	v_min_u32_e32 v134, v134, v76
	v_max_u32_e32 v76, v69, v74
	v_min_u32_e32 v139, v69, v74
	v_max_u32_e32 v140, v66, v67
	v_min_u32_e32 v141, v66, v67
	v_max_u32_e32 v142, v73, v68
	v_min_u32_e32 v143, v73, v68
	v_max_u32_e32 v66, v70, v97
	v_min_u32_e32 v67, v70, v97
	v_max_u32_e32 v68, v96, v135
	v_min_u32_e32 v69, v96, v135
	v_max_u32_e32 v70, v136, v77
	v_min_u32_e32 v71, v136, v77
	v_max_u32_e32 v72, v75, v137
	v_min_u32_e32 v73, v75, v137
	v_max_u32_e32 v74, v138, v76
	v_min_u32_e32 v75, v138, v76
	v_max_u32_e32 v76, v134, v139
	v_min_u32_e32 v77, v134, v139
	v_max_u32_e32 v96, v140, v142
	v_min_u32_e32 v97, v140, v142
	v_max_u32_e32 v134, v141, v143
	v_min_u32_e32 v135, v141, v143
	v_mov_b32_e32 v136, v66
	v_mov_b32_e32 v137, v67
	v_mov_b32_e32 v138, v68
	v_mov_b32_e32 v139, v69
	v_mov_b32_e32 v140, v70
	v_mov_b32_e32 v141, v71
	v_mov_b32_e32 v142, v72
	v_mov_b32_e32 v143, v73
	v_mov_b32_e32 v144, v74
	v_mov_b32_e32 v145, v75
	v_mov_b32_e32 v146, v76
	v_mov_b32_e32 v147, v77
	v_mov_b32_e32 v148, v96
	v_mov_b32_e32 v149, v97
	v_mov_b32_e32 v150, v134
	v_mov_b32_e32 v151, v135
	v_permlane32_swap_b32_e32 v66, v136
	v_permlane32_swap_b32_e32 v67, v137
	v_permlane32_swap_b32_e32 v68, v138
	v_permlane32_swap_b32_e32 v69, v139
	v_permlane32_swap_b32_e32 v70, v140
	v_permlane32_swap_b32_e32 v71, v141
	v_permlane32_swap_b32_e32 v72, v142
	v_permlane32_swap_b32_e32 v73, v143
	v_permlane32_swap_b32_e32 v74, v144
	v_permlane32_swap_b32_e32 v75, v145
	v_permlane32_swap_b32_e32 v76, v146
	v_permlane32_swap_b32_e32 v77, v147
	v_permlane32_swap_b32_e32 v96, v148
	v_permlane32_swap_b32_e32 v97, v149
	v_permlane32_swap_b32_e32 v134, v150
	v_permlane32_swap_b32_e32 v135, v151
	s_and_saveexec_b64 s[0:1], s[40:41]
	s_cbranch_execz .LBB0_739
	ds_write_b128 v83, v[34:37]
	ds_write_b128 v83, v[38:41] offset:64
	ds_write_b128 v83, v[54:57] offset:16
	ds_write_b128 v83, v[42:45] offset:80
	ds_write_b128 v83, v[58:61] offset:32
	ds_write_b128 v83, v[46:49] offset:96
	ds_write_b128 v83, v[62:65] offset:48
	ds_write_b128 v83, v[50:53] offset:112
